# baseline (speedup 1.0000x reference)
.Lmy_noperm_in:
	v_mfma_f32_16x16x32_f16 v[210:213], v[70:73], v[150:153], v[98:101]
	v_mfma_f32_16x16x32_f16 v[214:217], v[74:77], v[150:153], v[102:105]
	v_mfma_f32_16x16x32_f16 v[210:213], v[66:69], v[154:157], v[210:213]
	v_mfma_f32_16x16x32_f16 v[214:217], v[78:81], v[154:157], v[214:217]
	s_add_u32 s48, s20, 0x600000
	s_addc_u32 s49, s21, 0
	s_sub_u32 s50, s22, 0x600000
	s_mov_b32 s51, s23
	s_add_u32 s68, s16, 0xc000
	s_addc_u32 s69, s17, 0
	s_sub_u32 s70, s18, 0xc000
	s_mov_b32 s71, s19
	s_add_u32 s52, s20, 0x700000
	s_addc_u32 s53, s21, 0
	s_sub_u32 s54, s22, 0x700000
	s_mov_b32 s55, s23
	s_add_u32 s72, s16, 0x10000
	s_addc_u32 s73, s17, 0
	s_sub_u32 s74, s18, 0x10000
	s_mov_b32 s75, s19
	s_add_u32 s56, s20, 0x800000
	s_addc_u32 s57, s21, 0
	s_sub_u32 s58, s22, 0x800000
	s_mov_b32 s59, s23
	s_add_u32 s76, s16, 0x14000
	s_addc_u32 s77, s17, 0
	s_sub_u32 s78, s18, 0x14000
	s_mov_b32 s79, s19
	s_add_u32 s60, s20, 0x900000
	s_addc_u32 s61, s21, 0
	s_sub_u32 s62, s22, 0x900000
	s_mov_b32 s63, s23
	s_add_u32 s80, s16, 0x18000
	s_addc_u32 s81, s17, 0
	s_sub_u32 s82, s18, 0x18000
	s_mov_b32 s83, s19
	v_mfma_f32_16x16x32_f16 v[218:221], v[82:85], v[150:153], v[106:109]
	v_mfma_f32_16x16x32_f16 v[222:225], v[90:93], v[150:153], v[110:113]
	v_mfma_f32_16x16x32_f16 v[218:221], v[86:89], v[154:157], v[218:221]
	v_mfma_f32_16x16x32_f16 v[222:225], v[94:97], v[154:157], v[222:225]
	s_waitcnt lgkmcnt(2)
	s_waitcnt lgkmcnt(0)
	s_waitcnt vmcnt(9)
	v_cvt_pk_f16_f32 v251, v196, v197
	ds_write_b32 v1, v251 offset:4096
	ds_read_b128 v[150:153], v186 offset:2048
	ds_read_b128 v[154:157], v186 offset:3072
	s_add_i32 s45, s45, 0x100000
	s_add_i32 s46, s46, 0x4000
	s_movk_i32 s47, 0x0
	s_add_i32 s43, s40, -12
	s_lshl_b32 s43, s43, 12
	s_cmp_lt_u32 s40, 14
	s_cselect_b32 s43, s47, s43
	v_exp_f32_e32 v226, v210
	v_exp_f32_e32 v227, v211
	v_min_f32_e32 v228, s42, v212
	v_exp_f32_e32 v229, v213
	v_exp_f32_e32 v228, v228
	v_add_f32_e32 v227, 1.0, v227
	v_fma_f32 v230, v228, s41, s41
	v_rcp_f32_e32 v227, v227
	v_fma_f32 v230, v226, v230, v230
	v_rcp_f32_e32 v230, v230
	s_nop 0
	v_fma_f32 v226, -v228, v230, v230
	v_fma_f32 v200, v200, v227, v226
	v_min_f32_e32 v226, s42, v200
	v_exp_f32_e32 v226, v226
	s_nop 0
	v_add_f32_e32 v227, 1.0, v226
	v_fma_f32 v227, v229, v227, v227
	v_rcp_f32_e32 v227, v227
	v_exp_f32_e32 v231, v214
	v_exp_f32_e32 v232, v215
	v_fma_mixlo_f16 v246, -v226, v227, v227
	v_min_f32_e32 v233, s42, v216
	v_exp_f32_e32 v234, v217
	v_exp_f32_e32 v236, v218
	v_exp_f32_e32 v233, v233
	v_add_f32_e32 v232, 1.0, v232
	v_exp_f32_e32 v227, v219
	v_fma_f32 v235, v233, s41, s41
	v_rcp_f32_e32 v232, v232
	v_min_f32_e32 v228, s42, v220
	v_fma_f32 v235, v231, v235, v235
	v_rcp_f32_e32 v235, v235
	v_exp_f32_e32 v229, v221
	v_fma_f32 v231, -v233, v235, v235
	v_fma_f32 v201, v201, v232, v231
	v_exp_f32_e32 v228, v228
	v_min_f32_e32 v231, s42, v201
	v_exp_f32_e32 v231, v231
	v_add_f32_e32 v227, 1.0, v227
	v_add_f32_e32 v232, 1.0, v231
	v_fma_f32 v232, v234, v232, v232
	v_fma_f32 v230, v228, s41, s41
	v_rcp_f32_e32 v232, v232
	s_nop 0
	v_fma_mixhi_f16 v246, -v231, v232, v232
	v_rcp_f32_e32 v227, v227
	v_exp_f32_e32 v231, v222
	buffer_load_dwordx4 v[138:141], v189, s[16:19], s46 offen
	buffer_load_dwordx4 v[142:145], v208, s[16:19], s46 offen
	v_exp_f32_e32 v232, v223
	v_fma_f32 v230, v236, v230, v230
	v_min_f32_e32 v233, s42, v224
	s_waitcnt lgkmcnt(0)
	v_mfma_f32_16x16x32_f16 v[210:213], v[70:73], v[150:153], v[98:101]
	v_exp_f32_e32 v234, v225
	v_rcp_f32_e32 v230, v230
	v_exp_f32_e32 v233, v233
	v_mfma_f32_16x16x32_f16 v[214:217], v[74:77], v[150:153], v[102:105]
	v_add_f32_e32 v232, 1.0, v232
	v_fma_f32 v236, -v228, v230, v230
	v_fma_f32 v235, v233, s41, s41
	v_rcp_f32_e32 v232, v232
	v_fma_f32 v198, v198, v227, v236
	v_fma_f32 v235, v231, v235, v235
	v_rcp_f32_e32 v235, v235
	v_min_f32_e32 v236, s42, v198
	v_fma_f32 v231, -v233, v235, v235
	v_fma_f32 v199, v199, v232, v231
	v_exp_f32_e32 v236, v236
	v_min_f32_e32 v231, s42, v199
	v_exp_f32_e32 v231, v231
	v_add_f32_e32 v227, 1.0, v236
	v_add_f32_e32 v232, 1.0, v231
	v_fma_f32 v227, v229, v227, v227
	v_fma_f32 v232, v234, v232, v232
	v_rcp_f32_e32 v227, v227
	v_rcp_f32_e32 v232, v232
	v_fma_mixlo_f16 v247, -v236, v227, v227
	v_fma_mixhi_f16 v247, -v231, v232, v232
	ds_write_b64 v206, v[246:247] offset:8192
	v_mfma_f32_16x16x32_f16 v[210:213], v[66:69], v[154:157], v[210:213]
	v_mfma_f32_16x16x32_f16 v[214:217], v[78:81], v[154:157], v[214:217]
	v_mov_b32_e32 v174, v246
	v_mov_b32_e32 v175, v247
	buffer_load_dwordx2 v[196:197], v209, s[20:23], s45 offen
	s_add_i32 s40, s40, 1
	s_add_i32 s44, s44, 0x1000
	s_waitcnt lgkmcnt(0)
	s_barrier
	ds_read_b128 v[158:161], v252 offset:0
	ds_read_b128 v[162:165], v252 offset:1024
	ds_read_b128 v[166:169], v253 offset:2048
	ds_read_b128 v[170:173], v253 offset:3072
	v_mfma_f32_16x16x32_f16 v[218:221], v[82:85], v[150:153], v[106:109]
	v_mfma_f32_16x16x32_f16 v[222:225], v[90:93], v[150:153], v[110:113]
	v_mfma_f32_16x16x32_f16 v[218:221], v[86:89], v[154:157], v[218:221]
	v_mfma_f32_16x16x32_f16 v[222:225], v[94:97], v[154:157], v[222:225]
	s_waitcnt lgkmcnt(2)
	v_mfma_f32_16x16x32_f16 v[210:213], v[54:57], v[158:161], v[210:213]
	v_mfma_f32_16x16x32_f16 v[210:213], v[58:61], v[162:165], v[210:213]
	s_waitcnt lgkmcnt(0)
	v_mfma_f32_16x16x32_f16 v[210:213], v[62:65], v[166:169], v[210:213]
	v_mfma_f32_16x16x32_f16 v[210:213], v[50:53], v[170:173], v[210:213]
	s_waitcnt vmcnt(9)
	v_cvt_pk_f16_f32 v251, v194, v195
	ds_write_b32 v1, v251 offset:6144
	ds_read_b128 v[150:153], v186 offset:4096
	ds_read_b128 v[154:157], v186 offset:5120
	s_add_i32 s45, s45, 0x100000
	s_add_i32 s46, s46, 0x4000
	s_movk_i32 s47, 0x1000
	s_add_i32 s43, s40, -12
	s_lshl_b32 s43, s43, 12
	s_cmp_lt_u32 s40, 14
	s_cselect_b32 s43, s47, s43
	v_exp_f32_e32 v226, v210
	v_exp_f32_e32 v227, v211
	v_mfma_f32_16x16x32_f16 v[214:217], v[34:37], v[158:161], v[214:217]
	v_min_f32_e32 v228, s42, v212
	v_exp_f32_e32 v229, v213
	v_mfma_f32_16x16x32_f16 v[214:217], v[38:41], v[162:165], v[214:217]
	v_exp_f32_e32 v228, v228
	v_add_f32_e32 v227, 1.0, v227
	v_mfma_f32_16x16x32_f16 v[214:217], v[42:45], v[166:169], v[214:217]
	v_fma_f32 v230, v228, s41, s41
	v_rcp_f32_e32 v227, v227
	v_mfma_f32_16x16x32_f16 v[214:217], v[46:49], v[170:173], v[214:217]
	v_fma_f32 v230, v226, v230, v230
	v_rcp_f32_e32 v230, v230
	v_mfma_f32_16x16x32_f16 v[218:221], v[18:21], v[158:161], v[218:221]
	v_fma_f32 v226, -v228, v230, v230
	v_fma_f32 v200, v200, v227, v226
	v_mfma_f32_16x16x32_f16 v[218:221], v[14:17], v[162:165], v[218:221]
	v_min_f32_e32 v226, s42, v200
	v_exp_f32_e32 v226, v226
	v_mfma_f32_16x16x32_f16 v[218:221], v[10:13], v[166:169], v[218:221]
	v_add_f32_e32 v227, 1.0, v226
	v_fma_f32 v227, v229, v227, v227
	v_mfma_f32_16x16x32_f16 v[218:221], v[26:29], v[170:173], v[218:221]
	v_rcp_f32_e32 v227, v227
	v_exp_f32_e32 v231, v214
	v_mfma_f32_16x16x32_f16 v[222:225], v[2:5], v[158:161], v[222:225]
	v_exp_f32_e32 v232, v215
	v_fma_mixlo_f16 v246, -v226, v227, v227
	v_mfma_f32_16x16x32_f16 v[222:225], v[6:9], v[162:165], v[222:225]
	v_min_f32_e32 v233, s42, v216
	v_exp_f32_e32 v234, v217
	v_mfma_f32_16x16x32_f16 v[222:225], v[22:25], v[166:169], v[222:225]
	v_exp_f32_e32 v236, v218
	v_exp_f32_e32 v233, v233
	v_mfma_f32_16x16x32_f16 v[222:225], v[30:33], v[170:173], v[222:225]
	v_add_f32_e32 v232, 1.0, v232
	v_exp_f32_e32 v227, v219
	v_fma_f32 v235, v233, s41, s41
	v_rcp_f32_e32 v232, v232
	v_min_f32_e32 v228, s42, v220
	v_fma_f32 v235, v231, v235, v235
	v_rcp_f32_e32 v235, v235
	v_exp_f32_e32 v229, v221
	v_fma_f32 v231, -v233, v235, v235
	v_fma_f32 v201, v201, v232, v231
	v_exp_f32_e32 v228, v228
	v_min_f32_e32 v231, s42, v201
	v_exp_f32_e32 v231, v231
	v_add_f32_e32 v227, 1.0, v227
	v_add_f32_e32 v232, 1.0, v231
	v_mfma_f32_16x16x32_f16 v[146:149], v[130:133], v[158:161], v[146:149]
	v_fma_f32 v232, v234, v232, v232
	v_fma_f32 v230, v228, s41, s41
	v_rcp_f32_e32 v232, v232
	v_mfma_f32_16x16x32_f16 v[146:149], v[134:137], v[162:165], v[146:149]
	v_fma_mixhi_f16 v246, -v231, v232, v232
	v_rcp_f32_e32 v227, v227
	v_exp_f32_e32 v231, v222
	buffer_load_dwordx4 v[130:133], v189, s[16:19], s46 offen
	buffer_load_dwordx4 v[134:137], v208, s[16:19], s46 offen
	v_exp_f32_e32 v232, v223
	v_fma_f32 v230, v236, v230, v230
	v_min_f32_e32 v233, s42, v224
	s_waitcnt lgkmcnt(0)
	v_mfma_f32_16x16x32_f16 v[210:213], v[70:73], v[150:153], v[98:101]
	v_exp_f32_e32 v234, v225
	v_rcp_f32_e32 v230, v230
	v_exp_f32_e32 v233, v233
	v_mfma_f32_16x16x32_f16 v[214:217], v[74:77], v[150:153], v[102:105]
	v_add_f32_e32 v232, 1.0, v232
	v_fma_f32 v236, -v228, v230, v230
	v_fma_f32 v235, v233, s41, s41
	v_rcp_f32_e32 v232, v232
	v_fma_f32 v198, v198, v227, v236
	v_fma_f32 v235, v231, v235, v235
	v_rcp_f32_e32 v235, v235
	v_min_f32_e32 v236, s42, v198
	v_fma_f32 v231, -v233, v235, v235
	v_fma_f32 v199, v199, v232, v231
	v_exp_f32_e32 v236, v236
	v_min_f32_e32 v231, s42, v199
	v_exp_f32_e32 v231, v231
	v_add_f32_e32 v227, 1.0, v236
	v_add_f32_e32 v232, 1.0, v231
	v_fma_f32 v227, v229, v227, v227
	v_fma_f32 v232, v234, v232, v232
	v_rcp_f32_e32 v227, v227
	v_rcp_f32_e32 v232, v232
	v_fma_mixlo_f16 v247, -v236, v227, v227
	v_fma_mixhi_f16 v247, -v231, v232, v232
	ds_write_b64 v206, v[246:247] offset:12288
	v_mfma_f32_16x16x32_f16 v[210:213], v[66:69], v[154:157], v[210:213]
	v_mfma_f32_16x16x32_f16 v[214:217], v[78:81], v[154:157], v[214:217]
	v_mov_b32_e32 v176, v246
	v_mov_b32_e32 v177, v247
	buffer_load_dwordx2 v[194:195], v209, s[20:23], s45 offen
	s_add_i32 s40, s40, 1
	s_add_i32 s44, s44, 0x1000
	s_waitcnt lgkmcnt(0)
	s_barrier
	ds_read_b128 v[158:161], v252 offset:4096
	ds_read_b128 v[162:165], v252 offset:5120
	ds_read_b128 v[166:169], v253 offset:6144
	ds_read_b128 v[170:173], v253 offset:7168
	v_mfma_f32_16x16x32_f16 v[218:221], v[82:85], v[150:153], v[106:109]
	v_mfma_f32_16x16x32_f16 v[222:225], v[90:93], v[150:153], v[110:113]
	v_mfma_f32_16x16x32_f16 v[218:221], v[86:89], v[154:157], v[218:221]
	v_mfma_f32_16x16x32_f16 v[222:225], v[94:97], v[154:157], v[222:225]
	s_waitcnt lgkmcnt(2)
	v_mfma_f32_16x16x32_f16 v[210:213], v[54:57], v[158:161], v[210:213]
	v_mfma_f32_16x16x32_f16 v[210:213], v[58:61], v[162:165], v[210:213]
	s_waitcnt lgkmcnt(0)
	v_mfma_f32_16x16x32_f16 v[210:213], v[62:65], v[166:169], v[210:213]
	v_mfma_f32_16x16x32_f16 v[210:213], v[50:53], v[170:173], v[210:213]
	s_waitcnt vmcnt(9)
	v_cvt_pk_f16_f32 v251, v192, v193
	ds_write_b32 v1, v251 offset:0
	ds_read_b128 v[150:153], v186 offset:6144
	ds_read_b128 v[154:157], v186 offset:7168
	s_add_i32 s45, s45, 0x100000
	s_add_i32 s46, s46, 0x4000
	s_movk_i32 s47, 0x0
	s_add_i32 s43, s40, -12
	s_lshl_b32 s43, s43, 12
	s_cmp_lt_u32 s40, 14
	s_cselect_b32 s43, s47, s43
	v_exp_f32_e32 v226, v210
	v_exp_f32_e32 v227, v211
	v_mfma_f32_16x16x32_f16 v[214:217], v[34:37], v[158:161], v[214:217]
	v_min_f32_e32 v228, s42, v212
	v_exp_f32_e32 v229, v213
	v_mfma_f32_16x16x32_f16 v[214:217], v[38:41], v[162:165], v[214:217]
	v_exp_f32_e32 v228, v228
	v_add_f32_e32 v227, 1.0, v227
	v_mfma_f32_16x16x32_f16 v[214:217], v[42:45], v[166:169], v[214:217]
	v_fma_f32 v230, v228, s41, s41
	v_rcp_f32_e32 v227, v227
	v_mfma_f32_16x16x32_f16 v[214:217], v[46:49], v[170:173], v[214:217]
	v_fma_f32 v230, v226, v230, v230
	v_rcp_f32_e32 v230, v230
	v_mfma_f32_16x16x32_f16 v[218:221], v[18:21], v[158:161], v[218:221]
	v_fma_f32 v226, -v228, v230, v230
	v_fma_f32 v200, v200, v227, v226
	v_mfma_f32_16x16x32_f16 v[218:221], v[14:17], v[162:165], v[218:221]
	v_min_f32_e32 v226, s42, v200
	v_exp_f32_e32 v226, v226
	v_mfma_f32_16x16x32_f16 v[218:221], v[10:13], v[166:169], v[218:221]
	v_add_f32_e32 v227, 1.0, v226
	v_fma_f32 v227, v229, v227, v227
	v_mfma_f32_16x16x32_f16 v[218:221], v[26:29], v[170:173], v[218:221]
	v_rcp_f32_e32 v227, v227
	v_exp_f32_e32 v231, v214
	v_mfma_f32_16x16x32_f16 v[222:225], v[2:5], v[158:161], v[222:225]
	v_exp_f32_e32 v232, v215
	v_fma_mixlo_f16 v246, -v226, v227, v227
	v_mfma_f32_16x16x32_f16 v[222:225], v[6:9], v[162:165], v[222:225]
	v_min_f32_e32 v233, s42, v216
	v_exp_f32_e32 v234, v217
	v_mfma_f32_16x16x32_f16 v[222:225], v[22:25], v[166:169], v[222:225]
	v_exp_f32_e32 v236, v218
	v_exp_f32_e32 v233, v233
	v_mfma_f32_16x16x32_f16 v[222:225], v[30:33], v[170:173], v[222:225]
	v_add_f32_e32 v232, 1.0, v232
	v_exp_f32_e32 v227, v219
	v_fma_f32 v235, v233, s41, s41
	v_rcp_f32_e32 v232, v232
	v_min_f32_e32 v228, s42, v220
	v_fma_f32 v235, v231, v235, v235
	v_rcp_f32_e32 v235, v235
	v_exp_f32_e32 v229, v221
	v_fma_f32 v231, -v233, v235, v235
	v_fma_f32 v201, v201, v232, v231
	v_exp_f32_e32 v228, v228
	v_min_f32_e32 v231, s42, v201
	v_exp_f32_e32 v231, v231
	v_add_f32_e32 v227, 1.0, v227
	v_add_f32_e32 v232, 1.0, v231
	v_mfma_f32_16x16x32_f16 v[146:149], v[122:125], v[158:161], v[146:149]
	v_fma_f32 v232, v234, v232, v232
	v_fma_f32 v230, v228, s41, s41
	v_rcp_f32_e32 v232, v232
	v_mfma_f32_16x16x32_f16 v[146:149], v[126:129], v[162:165], v[146:149]
	v_fma_mixhi_f16 v246, -v231, v232, v232
	v_rcp_f32_e32 v227, v227
	v_exp_f32_e32 v231, v222
	buffer_load_dwordx4 v[122:125], v189, s[16:19], s46 offen
	buffer_load_dwordx4 v[126:129], v208, s[16:19], s46 offen
	v_exp_f32_e32 v232, v223
	v_fma_f32 v230, v236, v230, v230
	v_min_f32_e32 v233, s42, v224
	s_waitcnt lgkmcnt(0)
	v_mfma_f32_16x16x32_f16 v[210:213], v[70:73], v[150:153], v[98:101]
	v_exp_f32_e32 v234, v225
	v_rcp_f32_e32 v230, v230
	v_exp_f32_e32 v233, v233
	v_mfma_f32_16x16x32_f16 v[214:217], v[74:77], v[150:153], v[102:105]
	v_add_f32_e32 v232, 1.0, v232
	v_fma_f32 v236, -v228, v230, v230
	v_fma_f32 v235, v233, s41, s41
	v_rcp_f32_e32 v232, v232
	v_fma_f32 v198, v198, v227, v236
	v_fma_f32 v235, v231, v235, v235
	v_rcp_f32_e32 v235, v235
	v_min_f32_e32 v236, s42, v198
	v_fma_f32 v231, -v233, v235, v235
	v_fma_f32 v199, v199, v232, v231
	v_exp_f32_e32 v236, v236
	v_min_f32_e32 v231, s42, v199
	v_exp_f32_e32 v231, v231
	v_add_f32_e32 v227, 1.0, v236
	v_add_f32_e32 v232, 1.0, v231
	v_fma_f32 v227, v229, v227, v227
	v_fma_f32 v232, v234, v232, v232
	v_rcp_f32_e32 v227, v227
	v_rcp_f32_e32 v232, v232
	v_fma_mixlo_f16 v247, -v236, v227, v227
	v_fma_mixhi_f16 v247, -v231, v232, v232
	ds_write_b64 v206, v[246:247] offset:8192
	v_mfma_f32_16x16x32_f16 v[210:213], v[66:69], v[154:157], v[210:213]
	v_mfma_f32_16x16x32_f16 v[214:217], v[78:81], v[154:157], v[214:217]
	v_mov_b32_e32 v178, v246
	v_mov_b32_e32 v179, v247
	buffer_load_dwordx2 v[192:193], v209, s[20:23], s45 offen
	s_add_i32 s40, s40, 1
	s_add_i32 s44, s44, 0x1000
	s_waitcnt lgkmcnt(0)
	s_barrier
	ds_read_b128 v[158:161], v252 offset:0
	ds_read_b128 v[162:165], v252 offset:1024
	ds_read_b128 v[166:169], v253 offset:2048
	ds_read_b128 v[170:173], v253 offset:3072
	v_mfma_f32_16x16x32_f16 v[218:221], v[82:85], v[150:153], v[106:109]
	v_mfma_f32_16x16x32_f16 v[222:225], v[90:93], v[150:153], v[110:113]
	v_mfma_f32_16x16x32_f16 v[218:221], v[86:89], v[154:157], v[218:221]
	v_mfma_f32_16x16x32_f16 v[222:225], v[94:97], v[154:157], v[222:225]
	s_waitcnt lgkmcnt(2)
	v_mfma_f32_16x16x32_f16 v[210:213], v[54:57], v[158:161], v[210:213]
	v_mfma_f32_16x16x32_f16 v[210:213], v[58:61], v[162:165], v[210:213]
	s_waitcnt lgkmcnt(0)
	v_mfma_f32_16x16x32_f16 v[210:213], v[62:65], v[166:169], v[210:213]
	v_mfma_f32_16x16x32_f16 v[210:213], v[50:53], v[170:173], v[210:213]
	s_waitcnt vmcnt(9)
	v_cvt_pk_f16_f32 v251, v190, v191
	ds_write_b32 v1, v251 offset:2048
	ds_read_b128 v[150:153], v186 offset:0
	ds_read_b128 v[154:157], v186 offset:1024
	s_add_i32 s45, s45, 0x100000
	s_add_i32 s46, s46, 0x4000
	s_movk_i32 s47, 0x1000
	s_add_i32 s43, s40, -12
	s_lshl_b32 s43, s43, 12
	s_cmp_lt_u32 s40, 14
	s_cselect_b32 s43, s47, s43
	v_exp_f32_e32 v226, v210
	v_exp_f32_e32 v227, v211
	v_mfma_f32_16x16x32_f16 v[214:217], v[34:37], v[158:161], v[214:217]
	v_min_f32_e32 v228, s42, v212
	v_exp_f32_e32 v229, v213
	v_mfma_f32_16x16x32_f16 v[214:217], v[38:41], v[162:165], v[214:217]
	v_exp_f32_e32 v228, v228
	v_add_f32_e32 v227, 1.0, v227
	v_mfma_f32_16x16x32_f16 v[214:217], v[42:45], v[166:169], v[214:217]
	v_fma_f32 v230, v228, s41, s41
	v_rcp_f32_e32 v227, v227
	v_mfma_f32_16x16x32_f16 v[214:217], v[46:49], v[170:173], v[214:217]
	v_fma_f32 v230, v226, v230, v230
	v_rcp_f32_e32 v230, v230
	v_mfma_f32_16x16x32_f16 v[218:221], v[18:21], v[158:161], v[218:221]
	v_fma_f32 v226, -v228, v230, v230
	v_fma_f32 v200, v200, v227, v226
	v_mfma_f32_16x16x32_f16 v[218:221], v[14:17], v[162:165], v[218:221]
	v_min_f32_e32 v226, s42, v200
	v_exp_f32_e32 v226, v226
	v_mfma_f32_16x16x32_f16 v[218:221], v[10:13], v[166:169], v[218:221]
	v_add_f32_e32 v227, 1.0, v226
	v_fma_f32 v227, v229, v227, v227
	v_mfma_f32_16x16x32_f16 v[218:221], v[26:29], v[170:173], v[218:221]
	v_rcp_f32_e32 v227, v227
	v_exp_f32_e32 v231, v214
	v_mfma_f32_16x16x32_f16 v[222:225], v[2:5], v[158:161], v[222:225]
	v_exp_f32_e32 v232, v215
	v_fma_mixlo_f16 v246, -v226, v227, v227
	v_mfma_f32_16x16x32_f16 v[222:225], v[6:9], v[162:165], v[222:225]
	v_min_f32_e32 v233, s42, v216
	v_exp_f32_e32 v234, v217
	v_mfma_f32_16x16x32_f16 v[222:225], v[22:25], v[166:169], v[222:225]
	v_exp_f32_e32 v236, v218
	v_exp_f32_e32 v233, v233
	v_mfma_f32_16x16x32_f16 v[222:225], v[30:33], v[170:173], v[222:225]
	v_add_f32_e32 v232, 1.0, v232
	v_exp_f32_e32 v227, v219
	v_fma_f32 v235, v233, s41, s41
	v_rcp_f32_e32 v232, v232
	v_min_f32_e32 v228, s42, v220
	v_fma_f32 v235, v231, v235, v235
	v_rcp_f32_e32 v235, v235
	v_exp_f32_e32 v229, v221
	v_fma_f32 v231, -v233, v235, v235
	v_fma_f32 v201, v201, v232, v231
	v_exp_f32_e32 v228, v228
	v_min_f32_e32 v231, s42, v201
	v_exp_f32_e32 v231, v231
	v_add_f32_e32 v227, 1.0, v227
	v_add_f32_e32 v232, 1.0, v231
	v_mfma_f32_16x16x32_f16 v[146:149], v[114:117], v[158:161], v[146:149]
	v_fma_f32 v232, v234, v232, v232
	v_fma_f32 v230, v228, s41, s41
	v_rcp_f32_e32 v232, v232
	v_mfma_f32_16x16x32_f16 v[146:149], v[118:121], v[162:165], v[146:149]
	v_fma_mixhi_f16 v246, -v231, v232, v232
	v_rcp_f32_e32 v227, v227
	v_exp_f32_e32 v231, v222
	buffer_load_dwordx4 v[114:117], v189, s[16:19], s46 offen
	buffer_load_dwordx4 v[118:121], v208, s[16:19], s46 offen
	v_exp_f32_e32 v232, v223
	v_fma_f32 v230, v236, v230, v230
	v_min_f32_e32 v233, s42, v224
	s_waitcnt lgkmcnt(0)
	v_mfma_f32_16x16x32_f16 v[210:213], v[70:73], v[150:153], v[98:101]
	v_exp_f32_e32 v234, v225
	v_rcp_f32_e32 v230, v230
	v_exp_f32_e32 v233, v233
	v_mfma_f32_16x16x32_f16 v[214:217], v[74:77], v[150:153], v[102:105]
	v_add_f32_e32 v232, 1.0, v232
	v_fma_f32 v236, -v228, v230, v230
	v_fma_f32 v235, v233, s41, s41
	v_rcp_f32_e32 v232, v232
	v_fma_f32 v198, v198, v227, v236
	v_fma_f32 v235, v231, v235, v235
	v_rcp_f32_e32 v235, v235
	v_min_f32_e32 v236, s42, v198
	v_fma_f32 v231, -v233, v235, v235
	v_fma_f32 v199, v199, v232, v231
	v_exp_f32_e32 v236, v236
	v_min_f32_e32 v231, s42, v199
	v_exp_f32_e32 v231, v231
	v_add_f32_e32 v227, 1.0, v236
	v_add_f32_e32 v232, 1.0, v231
	v_fma_f32 v227, v229, v227, v227
	v_fma_f32 v232, v234, v232, v232
	v_rcp_f32_e32 v227, v227
	v_rcp_f32_e32 v232, v232
	v_fma_mixlo_f16 v247, -v236, v227, v227
	v_fma_mixhi_f16 v247, -v231, v232, v232
	ds_write_b64 v206, v[246:247] offset:12288
	v_mfma_f32_16x16x32_f16 v[210:213], v[66:69], v[154:157], v[210:213]
	v_mfma_f32_16x16x32_f16 v[214:217], v[78:81], v[154:157], v[214:217]
	v_mov_b32_e32 v180, v246
	v_mov_b32_e32 v181, v247
	buffer_load_dwordx2 v[190:191], v209, s[20:23], s45 offen
	s_add_i32 s40, s40, 1
	s_add_i32 s44, s44, 0x1000
	s_waitcnt lgkmcnt(0)
	s_barrier
	ds_read_b128 v[158:161], v252 offset:4096
	ds_read_b128 v[162:165], v252 offset:5120
	ds_read_b128 v[166:169], v253 offset:6144
	ds_read_b128 v[170:173], v253 offset:7168
	v_mfma_f32_16x16x32_f16 v[218:221], v[82:85], v[150:153], v[106:109]
	v_mfma_f32_16x16x32_f16 v[222:225], v[90:93], v[150:153], v[110:113]
	v_mfma_f32_16x16x32_f16 v[218:221], v[86:89], v[154:157], v[218:221]
	v_mfma_f32_16x16x32_f16 v[222:225], v[94:97], v[154:157], v[222:225]
	s_waitcnt lgkmcnt(2)
	v_mfma_f32_16x16x32_f16 v[210:213], v[54:57], v[158:161], v[210:213]
	v_mfma_f32_16x16x32_f16 v[210:213], v[58:61], v[162:165], v[210:213]
	s_waitcnt lgkmcnt(0)
	v_mfma_f32_16x16x32_f16 v[210:213], v[62:65], v[166:169], v[210:213]
	v_mfma_f32_16x16x32_f16 v[210:213], v[50:53], v[170:173], v[210:213]
	s_waitcnt vmcnt(9)
	v_cvt_pk_f16_f32 v251, v196, v197
	ds_write_b32 v1, v251 offset:4096
	ds_read_b128 v[150:153], v186 offset:2048
	ds_read_b128 v[154:157], v186 offset:3072
	s_add_i32 s45, s45, 0x100000
	s_add_i32 s46, s46, 0x4000
	s_movk_i32 s47, 0x0
	s_add_i32 s43, s40, -12
	s_lshl_b32 s43, s43, 12
	s_cmp_lt_u32 s40, 14
	s_cselect_b32 s43, s47, s43
	v_exp_f32_e32 v226, v210
	v_exp_f32_e32 v227, v211
	v_mfma_f32_16x16x32_f16 v[214:217], v[34:37], v[158:161], v[214:217]
	v_min_f32_e32 v228, s42, v212
	v_exp_f32_e32 v229, v213
	v_mfma_f32_16x16x32_f16 v[214:217], v[38:41], v[162:165], v[214:217]
	v_exp_f32_e32 v228, v228
	v_add_f32_e32 v227, 1.0, v227
	v_mfma_f32_16x16x32_f16 v[214:217], v[42:45], v[166:169], v[214:217]
	v_fma_f32 v230, v228, s41, s41
	v_rcp_f32_e32 v227, v227
	v_mfma_f32_16x16x32_f16 v[214:217], v[46:49], v[170:173], v[214:217]
	v_fma_f32 v230, v226, v230, v230
	v_rcp_f32_e32 v230, v230
	v_mfma_f32_16x16x32_f16 v[218:221], v[18:21], v[158:161], v[218:221]
	v_fma_f32 v226, -v228, v230, v230
	v_fma_f32 v200, v200, v227, v226
	v_mfma_f32_16x16x32_f16 v[218:221], v[14:17], v[162:165], v[218:221]
	v_min_f32_e32 v226, s42, v200
	v_exp_f32_e32 v226, v226
	v_mfma_f32_16x16x32_f16 v[218:221], v[10:13], v[166:169], v[218:221]
	v_add_f32_e32 v227, 1.0, v226
	v_fma_f32 v227, v229, v227, v227
	v_mfma_f32_16x16x32_f16 v[218:221], v[26:29], v[170:173], v[218:221]
	v_rcp_f32_e32 v227, v227
	v_exp_f32_e32 v231, v214
	v_mfma_f32_16x16x32_f16 v[222:225], v[2:5], v[158:161], v[222:225]
	v_exp_f32_e32 v232, v215
	v_fma_mixlo_f16 v246, -v226, v227, v227
	v_mfma_f32_16x16x32_f16 v[222:225], v[6:9], v[162:165], v[222:225]
	v_min_f32_e32 v233, s42, v216
	v_exp_f32_e32 v234, v217
	v_mfma_f32_16x16x32_f16 v[222:225], v[22:25], v[166:169], v[222:225]
	v_exp_f32_e32 v236, v218
	v_exp_f32_e32 v233, v233
	v_mfma_f32_16x16x32_f16 v[222:225], v[30:33], v[170:173], v[222:225]
	v_add_f32_e32 v232, 1.0, v232
	v_exp_f32_e32 v227, v219
	v_fma_f32 v235, v233, s41, s41
	v_rcp_f32_e32 v232, v232
	v_min_f32_e32 v228, s42, v220
	v_fma_f32 v235, v231, v235, v235
	v_rcp_f32_e32 v235, v235
	v_exp_f32_e32 v229, v221
	v_fma_f32 v231, -v233, v235, v235
	v_fma_f32 v201, v201, v232, v231
	v_exp_f32_e32 v228, v228
	v_min_f32_e32 v231, s42, v201
	v_exp_f32_e32 v231, v231
	v_add_f32_e32 v227, 1.0, v227
	v_add_f32_e32 v232, 1.0, v231
	v_mfma_f32_16x16x32_f16 v[146:149], v[138:141], v[158:161], v[146:149]
	v_fma_f32 v232, v234, v232, v232
	v_fma_f32 v230, v228, s41, s41
	v_rcp_f32_e32 v232, v232
	v_mfma_f32_16x16x32_f16 v[146:149], v[142:145], v[162:165], v[146:149]
	v_fma_mixhi_f16 v246, -v231, v232, v232
	v_rcp_f32_e32 v227, v227
	v_exp_f32_e32 v231, v222
	buffer_load_dwordx4 v[138:141], v189, s[16:19], s46 offen
	buffer_load_dwordx4 v[142:145], v208, s[16:19], s46 offen
	v_exp_f32_e32 v232, v223
	v_fma_f32 v230, v236, v230, v230
	v_min_f32_e32 v233, s42, v224
	s_waitcnt lgkmcnt(0)
	v_mfma_f32_16x16x32_f16 v[210:213], v[70:73], v[150:153], v[98:101]
	v_exp_f32_e32 v234, v225
	v_rcp_f32_e32 v230, v230
	v_exp_f32_e32 v233, v233
	v_mfma_f32_16x16x32_f16 v[214:217], v[74:77], v[150:153], v[102:105]
	v_add_f32_e32 v232, 1.0, v232
	v_fma_f32 v236, -v228, v230, v230
	v_fma_f32 v235, v233, s41, s41
	v_rcp_f32_e32 v232, v232
	v_fma_f32 v198, v198, v227, v236
	v_fma_f32 v235, v231, v235, v235
	v_rcp_f32_e32 v235, v235
	v_min_f32_e32 v236, s42, v198
	v_fma_f32 v231, -v233, v235, v235
	v_fma_f32 v199, v199, v232, v231
	v_exp_f32_e32 v236, v236
	v_min_f32_e32 v231, s42, v199
	v_exp_f32_e32 v231, v231
	v_add_f32_e32 v227, 1.0, v236
	v_add_f32_e32 v232, 1.0, v231
	v_fma_f32 v227, v229, v227, v227
	v_fma_f32 v232, v234, v232, v232
	v_rcp_f32_e32 v227, v227
	v_rcp_f32_e32 v232, v232
	v_fma_mixlo_f16 v247, -v236, v227, v227
	v_fma_mixhi_f16 v247, -v231, v232, v232
	ds_write_b64 v206, v[246:247] offset:8192
	v_mfma_f32_16x16x32_f16 v[210:213], v[66:69], v[154:157], v[210:213]
	v_mfma_f32_16x16x32_f16 v[214:217], v[78:81], v[154:157], v[214:217]
	v_mov_b32_e32 v182, v246
	v_mov_b32_e32 v183, v247
	buffer_load_dwordx2 v[196:197], v209, s[20:23], s45 offen
	s_add_i32 s40, s40, 1
	s_add_i32 s44, s44, 0x1000
	s_waitcnt lgkmcnt(0)
	s_barrier
	ds_read_b128 v[158:161], v252 offset:0
	ds_read_b128 v[162:165], v252 offset:1024
	ds_read_b128 v[166:169], v253 offset:2048
	ds_read_b128 v[170:173], v253 offset:3072
	v_mfma_f32_16x16x32_f16 v[218:221], v[82:85], v[150:153], v[106:109]
	v_mfma_f32_16x16x32_f16 v[222:225], v[90:93], v[150:153], v[110:113]
	v_mfma_f32_16x16x32_f16 v[218:221], v[86:89], v[154:157], v[218:221]
	v_mfma_f32_16x16x32_f16 v[222:225], v[94:97], v[154:157], v[222:225]
	s_waitcnt lgkmcnt(2)
	v_mfma_f32_16x16x32_f16 v[210:213], v[54:57], v[158:161], v[210:213]
	v_mfma_f32_16x16x32_f16 v[210:213], v[58:61], v[162:165], v[210:213]
	s_waitcnt lgkmcnt(0)
	v_mfma_f32_16x16x32_f16 v[210:213], v[62:65], v[166:169], v[210:213]
	v_mfma_f32_16x16x32_f16 v[210:213], v[50:53], v[170:173], v[210:213]
	s_waitcnt vmcnt(9)
	v_cvt_pk_f16_f32 v251, v194, v195
	ds_write_b32 v1, v251 offset:6144
	ds_read_b128 v[150:153], v186 offset:4096
	ds_read_b128 v[154:157], v186 offset:5120
	s_add_i32 s45, s45, 0x100000
	s_add_i32 s46, s46, 0x4000
	s_movk_i32 s47, 0x1000
	s_add_i32 s43, s40, -12
	s_lshl_b32 s43, s43, 12
	s_cmp_lt_u32 s40, 14
	s_cselect_b32 s43, s47, s43
	v_exp_f32_e32 v226, v210
	v_exp_f32_e32 v227, v211
	v_mfma_f32_16x16x32_f16 v[214:217], v[34:37], v[158:161], v[214:217]
	v_min_f32_e32 v228, s42, v212
	v_exp_f32_e32 v229, v213
	v_mfma_f32_16x16x32_f16 v[214:217], v[38:41], v[162:165], v[214:217]
	v_exp_f32_e32 v228, v228
	v_add_f32_e32 v227, 1.0, v227
	v_mfma_f32_16x16x32_f16 v[214:217], v[42:45], v[166:169], v[214:217]
	v_fma_f32 v230, v228, s41, s41
	v_rcp_f32_e32 v227, v227
	v_mfma_f32_16x16x32_f16 v[214:217], v[46:49], v[170:173], v[214:217]
	v_fma_f32 v230, v226, v230, v230
	v_rcp_f32_e32 v230, v230
	v_mfma_f32_16x16x32_f16 v[218:221], v[18:21], v[158:161], v[218:221]
	v_fma_f32 v226, -v228, v230, v230
	v_fma_f32 v200, v200, v227, v226
	v_mfma_f32_16x16x32_f16 v[218:221], v[14:17], v[162:165], v[218:221]
	v_min_f32_e32 v226, s42, v200
	v_exp_f32_e32 v226, v226
	v_mfma_f32_16x16x32_f16 v[218:221], v[10:13], v[166:169], v[218:221]
	v_add_f32_e32 v227, 1.0, v226
	v_fma_f32 v227, v229, v227, v227
	v_mfma_f32_16x16x32_f16 v[218:221], v[26:29], v[170:173], v[218:221]
	v_rcp_f32_e32 v227, v227
	v_exp_f32_e32 v231, v214
	v_mfma_f32_16x16x32_f16 v[222:225], v[2:5], v[158:161], v[222:225]
	v_exp_f32_e32 v232, v215
	v_fma_mixlo_f16 v246, -v226, v227, v227
	v_mfma_f32_16x16x32_f16 v[222:225], v[6:9], v[162:165], v[222:225]
	v_min_f32_e32 v233, s42, v216
	v_exp_f32_e32 v234, v217
	v_mfma_f32_16x16x32_f16 v[222:225], v[22:25], v[166:169], v[222:225]
	v_exp_f32_e32 v236, v218
	v_exp_f32_e32 v233, v233
	v_mfma_f32_16x16x32_f16 v[222:225], v[30:33], v[170:173], v[222:225]
	v_add_f32_e32 v232, 1.0, v232
	v_exp_f32_e32 v227, v219
	v_fma_f32 v235, v233, s41, s41
	v_rcp_f32_e32 v232, v232
	v_min_f32_e32 v228, s42, v220
	v_fma_f32 v235, v231, v235, v235
	v_rcp_f32_e32 v235, v235
	v_exp_f32_e32 v229, v221
	v_fma_f32 v231, -v233, v235, v235
	v_fma_f32 v201, v201, v232, v231
	v_exp_f32_e32 v228, v228
	v_min_f32_e32 v231, s42, v201
	v_exp_f32_e32 v231, v231
	v_add_f32_e32 v227, 1.0, v227
	v_add_f32_e32 v232, 1.0, v231
	v_mfma_f32_16x16x32_f16 v[146:149], v[130:133], v[158:161], v[146:149]
	v_fma_f32 v232, v234, v232, v232
	v_fma_f32 v230, v228, s41, s41
	v_rcp_f32_e32 v232, v232
	v_mfma_f32_16x16x32_f16 v[146:149], v[134:137], v[162:165], v[146:149]
	v_fma_mixhi_f16 v246, -v231, v232, v232
	v_rcp_f32_e32 v227, v227
	v_exp_f32_e32 v231, v222
	buffer_load_dwordx4 v[130:133], v189, s[16:19], s46 offen
	buffer_load_dwordx4 v[134:137], v208, s[16:19], s46 offen
	v_exp_f32_e32 v232, v223
	v_fma_f32 v230, v236, v230, v230
	v_min_f32_e32 v233, s42, v224
	s_waitcnt lgkmcnt(0)
	v_mfma_f32_16x16x32_f16 v[210:213], v[70:73], v[150:153], v[98:101]
	v_exp_f32_e32 v234, v225
	v_rcp_f32_e32 v230, v230
	v_exp_f32_e32 v233, v233
	v_mfma_f32_16x16x32_f16 v[214:217], v[74:77], v[150:153], v[102:105]
	v_add_f32_e32 v232, 1.0, v232
	v_fma_f32 v236, -v228, v230, v230
	v_fma_f32 v235, v233, s41, s41
	v_rcp_f32_e32 v232, v232
	v_fma_f32 v198, v198, v227, v236
	v_fma_f32 v235, v231, v235, v235
	v_rcp_f32_e32 v235, v235
	v_min_f32_e32 v236, s42, v198
	v_fma_f32 v231, -v233, v235, v235
	v_fma_f32 v199, v199, v232, v231
	v_exp_f32_e32 v236, v236
	v_min_f32_e32 v231, s42, v199
	v_exp_f32_e32 v231, v231
	v_add_f32_e32 v227, 1.0, v236
	v_add_f32_e32 v232, 1.0, v231
	v_fma_f32 v227, v229, v227, v227
	v_fma_f32 v232, v234, v232, v232
	v_rcp_f32_e32 v227, v227
	v_rcp_f32_e32 v232, v232
	v_fma_mixlo_f16 v247, -v236, v227, v227
	v_fma_mixhi_f16 v247, -v231, v232, v232
	ds_write_b64 v206, v[246:247] offset:12288
	v_mfma_f32_16x16x32_f16 v[210:213], v[66:69], v[154:157], v[210:213]
	v_mfma_f32_16x16x32_f16 v[214:217], v[78:81], v[154:157], v[214:217]
	v_mov_b32_e32 v184, v246
	v_mov_b32_e32 v185, v247
	buffer_load_dwordx2 v[194:195], v209, s[20:23], s45 offen
	s_add_i32 s40, s40, 1
	s_add_i32 s44, s44, 0x1000
	s_waitcnt lgkmcnt(0)
	s_barrier
	ds_read_b128 v[158:161], v252 offset:4096
	ds_read_b128 v[162:165], v252 offset:5120
	ds_read_b128 v[166:169], v253 offset:6144
	ds_read_b128 v[170:173], v253 offset:7168
	v_mfma_f32_16x16x32_f16 v[218:221], v[82:85], v[150:153], v[106:109]
	v_mfma_f32_16x16x32_f16 v[222:225], v[90:93], v[150:153], v[110:113]
	v_mfma_f32_16x16x32_f16 v[218:221], v[86:89], v[154:157], v[218:221]
	v_mfma_f32_16x16x32_f16 v[222:225], v[94:97], v[154:157], v[222:225]
	s_waitcnt lgkmcnt(2)
	v_mfma_f32_16x16x32_f16 v[210:213], v[54:57], v[158:161], v[210:213]
	v_mfma_f32_16x16x32_f16 v[210:213], v[58:61], v[162:165], v[210:213]
	s_waitcnt lgkmcnt(0)
	v_mfma_f32_16x16x32_f16 v[210:213], v[62:65], v[166:169], v[210:213]
	v_mfma_f32_16x16x32_f16 v[210:213], v[50:53], v[170:173], v[210:213]
	s_waitcnt vmcnt(9)
	v_cvt_pk_f16_f32 v251, v192, v193
	ds_write_b32 v1, v251 offset:0
	ds_read_b128 v[150:153], v186 offset:6144
	ds_read_b128 v[154:157], v186 offset:7168
	s_add_i32 s45, s45, 0x100000
	s_add_i32 s46, s46, 0x4000
	s_movk_i32 s47, 0x0
	s_add_i32 s43, s40, -12
	s_lshl_b32 s43, s43, 12
	s_cmp_lt_u32 s40, 14
	s_cselect_b32 s43, s47, s43
	v_exp_f32_e32 v226, v210
	v_exp_f32_e32 v227, v211
	v_mfma_f32_16x16x32_f16 v[214:217], v[34:37], v[158:161], v[214:217]
	v_min_f32_e32 v228, s42, v212
	v_exp_f32_e32 v229, v213
	v_mfma_f32_16x16x32_f16 v[214:217], v[38:41], v[162:165], v[214:217]
	v_exp_f32_e32 v228, v228
	v_add_f32_e32 v227, 1.0, v227
	v_mfma_f32_16x16x32_f16 v[214:217], v[42:45], v[166:169], v[214:217]
	v_fma_f32 v230, v228, s41, s41
	v_rcp_f32_e32 v227, v227
	v_mfma_f32_16x16x32_f16 v[214:217], v[46:49], v[170:173], v[214:217]
	v_fma_f32 v230, v226, v230, v230
	v_rcp_f32_e32 v230, v230
	v_mfma_f32_16x16x32_f16 v[218:221], v[18:21], v[158:161], v[218:221]
	v_fma_f32 v226, -v228, v230, v230
	v_fma_f32 v200, v200, v227, v226
	v_mfma_f32_16x16x32_f16 v[218:221], v[14:17], v[162:165], v[218:221]
	v_min_f32_e32 v226, s42, v200
	v_exp_f32_e32 v226, v226
	v_mfma_f32_16x16x32_f16 v[218:221], v[10:13], v[166:169], v[218:221]
	v_add_f32_e32 v227, 1.0, v226
	v_fma_f32 v227, v229, v227, v227
	v_mfma_f32_16x16x32_f16 v[218:221], v[26:29], v[170:173], v[218:221]
	v_rcp_f32_e32 v227, v227
	v_exp_f32_e32 v231, v214
	v_mfma_f32_16x16x32_f16 v[222:225], v[2:5], v[158:161], v[222:225]
	v_exp_f32_e32 v232, v215
	v_fma_mixlo_f16 v246, -v226, v227, v227
	v_mfma_f32_16x16x32_f16 v[222:225], v[6:9], v[162:165], v[222:225]
	v_min_f32_e32 v233, s42, v216
	v_exp_f32_e32 v234, v217
	v_mfma_f32_16x16x32_f16 v[222:225], v[22:25], v[166:169], v[222:225]
	v_exp_f32_e32 v236, v218
	v_exp_f32_e32 v233, v233
	v_mfma_f32_16x16x32_f16 v[222:225], v[30:33], v[170:173], v[222:225]
	v_add_f32_e32 v232, 1.0, v232
	v_exp_f32_e32 v227, v219
	v_fma_f32 v235, v233, s41, s41
	v_rcp_f32_e32 v232, v232
	v_min_f32_e32 v228, s42, v220
	v_fma_f32 v235, v231, v235, v235
	v_rcp_f32_e32 v235, v235
	v_exp_f32_e32 v229, v221
	v_fma_f32 v231, -v233, v235, v235
	v_fma_f32 v201, v201, v232, v231
	v_exp_f32_e32 v228, v228
	v_min_f32_e32 v231, s42, v201
	v_exp_f32_e32 v231, v231
	v_add_f32_e32 v227, 1.0, v227
	v_add_f32_e32 v232, 1.0, v231
	v_mfma_f32_16x16x32_f16 v[146:149], v[122:125], v[158:161], v[146:149]
	v_fma_f32 v232, v234, v232, v232
	v_fma_f32 v230, v228, s41, s41
	v_rcp_f32_e32 v232, v232
	v_mfma_f32_16x16x32_f16 v[146:149], v[126:129], v[162:165], v[146:149]
	v_fma_mixhi_f16 v246, -v231, v232, v232
	v_rcp_f32_e32 v227, v227
	v_exp_f32_e32 v231, v222
	buffer_load_dwordx4 v[122:125], v189, s[16:19], s46 offen
	buffer_load_dwordx4 v[126:129], v208, s[16:19], s46 offen
	v_exp_f32_e32 v232, v223
	v_fma_f32 v230, v236, v230, v230
	v_min_f32_e32 v233, s42, v224
	s_waitcnt lgkmcnt(0)
	v_mfma_f32_16x16x32_f16 v[210:213], v[70:73], v[150:153], v[98:101]
	v_exp_f32_e32 v234, v225
	v_rcp_f32_e32 v230, v230
	v_exp_f32_e32 v233, v233
	v_mfma_f32_16x16x32_f16 v[214:217], v[74:77], v[150:153], v[102:105]
	v_add_f32_e32 v232, 1.0, v232
	v_fma_f32 v236, -v228, v230, v230
	v_fma_f32 v235, v233, s41, s41
	v_rcp_f32_e32 v232, v232
	v_fma_f32 v198, v198, v227, v236
	v_fma_f32 v235, v231, v235, v235
	v_rcp_f32_e32 v235, v235
	v_min_f32_e32 v236, s42, v198
	v_fma_f32 v231, -v233, v235, v235
	v_fma_f32 v199, v199, v232, v231
	v_exp_f32_e32 v236, v236
	v_min_f32_e32 v231, s42, v199
	v_exp_f32_e32 v231, v231
	v_add_f32_e32 v227, 1.0, v236
	v_add_f32_e32 v232, 1.0, v231
	v_fma_f32 v227, v229, v227, v227
	v_fma_f32 v232, v234, v232, v232
	v_rcp_f32_e32 v227, v227
	v_rcp_f32_e32 v232, v232
	v_fma_mixlo_f16 v247, -v236, v227, v227
	v_fma_mixhi_f16 v247, -v231, v232, v232
	ds_write_b64 v206, v[246:247] offset:8192
	v_mfma_f32_16x16x32_f16 v[210:213], v[66:69], v[154:157], v[210:213]
	v_mfma_f32_16x16x32_f16 v[214:217], v[78:81], v[154:157], v[214:217]
	v_mov_b32_e32 v237, v246
	v_mov_b32_e32 v238, v247
	buffer_load_dwordx2 v[192:193], v209, s[20:23], s45 offen
	s_add_i32 s40, s40, 1
	s_add_i32 s44, s44, 0x1000
	s_waitcnt lgkmcnt(0)
	s_barrier
	ds_read_b128 v[158:161], v252 offset:0
	ds_read_b128 v[162:165], v252 offset:1024
	ds_read_b128 v[166:169], v253 offset:2048
	ds_read_b128 v[170:173], v253 offset:3072
	v_mfma_f32_16x16x32_f16 v[218:221], v[82:85], v[150:153], v[106:109]
	v_mfma_f32_16x16x32_f16 v[222:225], v[90:93], v[150:153], v[110:113]
	v_mfma_f32_16x16x32_f16 v[218:221], v[86:89], v[154:157], v[218:221]
	v_mfma_f32_16x16x32_f16 v[222:225], v[94:97], v[154:157], v[222:225]
	s_waitcnt lgkmcnt(2)
	v_mfma_f32_16x16x32_f16 v[210:213], v[54:57], v[158:161], v[210:213]
	v_mfma_f32_16x16x32_f16 v[210:213], v[58:61], v[162:165], v[210:213]
	s_waitcnt lgkmcnt(0)
	v_mfma_f32_16x16x32_f16 v[210:213], v[62:65], v[166:169], v[210:213]
	v_mfma_f32_16x16x32_f16 v[210:213], v[50:53], v[170:173], v[210:213]
	s_waitcnt vmcnt(9)
	v_cvt_pk_f16_f32 v251, v190, v191
	ds_write_b32 v1, v251 offset:2048
	ds_read_b128 v[150:153], v186 offset:0
	ds_read_b128 v[154:157], v186 offset:1024
	s_add_i32 s45, s45, 0x100000
	s_add_i32 s46, s46, 0x4000
	s_movk_i32 s47, 0x1000
	s_add_i32 s43, s40, -12
	s_lshl_b32 s43, s43, 12
	s_cmp_lt_u32 s40, 14
	s_cselect_b32 s43, s47, s43
	v_exp_f32_e32 v226, v210
	v_exp_f32_e32 v227, v211
	v_mfma_f32_16x16x32_f16 v[214:217], v[34:37], v[158:161], v[214:217]
	v_min_f32_e32 v228, s42, v212
	v_exp_f32_e32 v229, v213
	v_mfma_f32_16x16x32_f16 v[214:217], v[38:41], v[162:165], v[214:217]
	v_exp_f32_e32 v228, v228
	v_add_f32_e32 v227, 1.0, v227
	v_mfma_f32_16x16x32_f16 v[214:217], v[42:45], v[166:169], v[214:217]
	v_fma_f32 v230, v228, s41, s41
	v_rcp_f32_e32 v227, v227
	v_mfma_f32_16x16x32_f16 v[214:217], v[46:49], v[170:173], v[214:217]
	v_fma_f32 v230, v226, v230, v230
	v_rcp_f32_e32 v230, v230
	v_mfma_f32_16x16x32_f16 v[218:221], v[18:21], v[158:161], v[218:221]
	v_fma_f32 v226, -v228, v230, v230
	v_fma_f32 v200, v200, v227, v226
	v_mfma_f32_16x16x32_f16 v[218:221], v[14:17], v[162:165], v[218:221]
	v_min_f32_e32 v226, s42, v200
	v_exp_f32_e32 v226, v226
	v_mfma_f32_16x16x32_f16 v[218:221], v[10:13], v[166:169], v[218:221]
	v_add_f32_e32 v227, 1.0, v226
	v_fma_f32 v227, v229, v227, v227
	v_mfma_f32_16x16x32_f16 v[218:221], v[26:29], v[170:173], v[218:221]
	v_rcp_f32_e32 v227, v227
	v_exp_f32_e32 v231, v214
	v_mfma_f32_16x16x32_f16 v[222:225], v[2:5], v[158:161], v[222:225]
	v_exp_f32_e32 v232, v215
	v_fma_mixlo_f16 v246, -v226, v227, v227
	v_mfma_f32_16x16x32_f16 v[222:225], v[6:9], v[162:165], v[222:225]
	v_min_f32_e32 v233, s42, v216
	v_exp_f32_e32 v234, v217
	v_mfma_f32_16x16x32_f16 v[222:225], v[22:25], v[166:169], v[222:225]
	v_exp_f32_e32 v236, v218
	v_exp_f32_e32 v233, v233
	v_mfma_f32_16x16x32_f16 v[222:225], v[30:33], v[170:173], v[222:225]
	v_add_f32_e32 v232, 1.0, v232
	v_exp_f32_e32 v227, v219
	v_fma_f32 v235, v233, s41, s41
	v_rcp_f32_e32 v232, v232
	v_min_f32_e32 v228, s42, v220
	v_fma_f32 v235, v231, v235, v235
	v_rcp_f32_e32 v235, v235
	v_exp_f32_e32 v229, v221
	v_fma_f32 v231, -v233, v235, v235
	v_fma_f32 v201, v201, v232, v231
	v_exp_f32_e32 v228, v228
	v_min_f32_e32 v231, s42, v201
	v_exp_f32_e32 v231, v231
	v_add_f32_e32 v227, 1.0, v227
	v_add_f32_e32 v232, 1.0, v231
	v_mfma_f32_16x16x32_f16 v[146:149], v[114:117], v[158:161], v[146:149]
	v_fma_f32 v232, v234, v232, v232
	v_fma_f32 v230, v228, s41, s41
	v_rcp_f32_e32 v232, v232
	v_mfma_f32_16x16x32_f16 v[146:149], v[118:121], v[162:165], v[146:149]
	v_fma_mixhi_f16 v246, -v231, v232, v232
	v_rcp_f32_e32 v227, v227
	v_exp_f32_e32 v231, v222
	buffer_load_dwordx4 v[114:117], v189, s[16:19], s46 offen
	buffer_load_dwordx4 v[118:121], v208, s[16:19], s46 offen
	v_exp_f32_e32 v232, v223
	v_fma_f32 v230, v236, v230, v230
	v_min_f32_e32 v233, s42, v224
	s_waitcnt lgkmcnt(0)
	v_mfma_f32_16x16x32_f16 v[210:213], v[70:73], v[150:153], v[98:101]
	v_exp_f32_e32 v234, v225
	v_rcp_f32_e32 v230, v230
	v_exp_f32_e32 v233, v233
	v_mfma_f32_16x16x32_f16 v[214:217], v[74:77], v[150:153], v[102:105]
	v_add_f32_e32 v232, 1.0, v232
	v_fma_f32 v236, -v228, v230, v230
	v_fma_f32 v235, v233, s41, s41
	v_rcp_f32_e32 v232, v232
	v_fma_f32 v198, v198, v227, v236
	v_fma_f32 v235, v231, v235, v235
	v_rcp_f32_e32 v235, v235
	v_min_f32_e32 v236, s42, v198
	v_fma_f32 v231, -v233, v235, v235
	v_fma_f32 v199, v199, v232, v231
	v_exp_f32_e32 v236, v236
	v_min_f32_e32 v231, s42, v199
	v_exp_f32_e32 v231, v231
	v_add_f32_e32 v227, 1.0, v236
	v_add_f32_e32 v232, 1.0, v231
	v_fma_f32 v227, v229, v227, v227
	v_fma_f32 v232, v234, v232, v232
	v_rcp_f32_e32 v227, v227
	v_rcp_f32_e32 v232, v232
	v_fma_mixlo_f16 v247, -v236, v227, v227
	v_fma_mixhi_f16 v247, -v231, v232, v232
	ds_write_b64 v206, v[246:247] offset:12288
	v_mfma_f32_16x16x32_f16 v[210:213], v[66:69], v[154:157], v[210:213]
	v_mfma_f32_16x16x32_f16 v[214:217], v[78:81], v[154:157], v[214:217]
	v_mov_b32_e32 v239, v246
	v_mov_b32_e32 v240, v247
	buffer_load_dwordx2 v[190:191], v209, s[20:23], s45 offen
	s_add_i32 s40, s40, 1
	s_add_i32 s44, s44, 0x1000
	s_waitcnt lgkmcnt(0)
	s_barrier
	ds_read_b128 v[158:161], v252 offset:4096
	ds_read_b128 v[162:165], v252 offset:5120
	ds_read_b128 v[166:169], v253 offset:6144
	ds_read_b128 v[170:173], v253 offset:7168
	v_mfma_f32_16x16x32_f16 v[218:221], v[82:85], v[150:153], v[106:109]
	v_mfma_f32_16x16x32_f16 v[222:225], v[90:93], v[150:153], v[110:113]
	v_mfma_f32_16x16x32_f16 v[218:221], v[86:89], v[154:157], v[218:221]
	v_mfma_f32_16x16x32_f16 v[222:225], v[94:97], v[154:157], v[222:225]
	s_waitcnt lgkmcnt(2)
	v_mfma_f32_16x16x32_f16 v[210:213], v[54:57], v[158:161], v[210:213]
	v_mfma_f32_16x16x32_f16 v[210:213], v[58:61], v[162:165], v[210:213]
	s_waitcnt lgkmcnt(0)
	v_mfma_f32_16x16x32_f16 v[210:213], v[62:65], v[166:169], v[210:213]
	v_mfma_f32_16x16x32_f16 v[210:213], v[50:53], v[170:173], v[210:213]
	s_waitcnt vmcnt(9)
	v_cvt_pk_f16_f32 v251, v196, v197
	ds_write_b32 v1, v251 offset:4096
	ds_read_b128 v[150:153], v186 offset:2048
	ds_read_b128 v[154:157], v186 offset:3072
	s_add_i32 s45, s45, 0x100000
	s_add_i32 s46, s46, 0x4000
	s_movk_i32 s47, 0x0
	s_add_i32 s43, s40, -12
	s_lshl_b32 s43, s43, 12
	s_cmp_lt_u32 s40, 14
	s_cselect_b32 s43, s47, s43
	v_exp_f32_e32 v226, v210
	v_exp_f32_e32 v227, v211
	v_mfma_f32_16x16x32_f16 v[214:217], v[34:37], v[158:161], v[214:217]
	v_min_f32_e32 v228, s42, v212
	v_exp_f32_e32 v229, v213
	v_mfma_f32_16x16x32_f16 v[214:217], v[38:41], v[162:165], v[214:217]
	v_exp_f32_e32 v228, v228
	v_add_f32_e32 v227, 1.0, v227
	v_mfma_f32_16x16x32_f16 v[214:217], v[42:45], v[166:169], v[214:217]
	v_fma_f32 v230, v228, s41, s41
	v_rcp_f32_e32 v227, v227
	v_mfma_f32_16x16x32_f16 v[214:217], v[46:49], v[170:173], v[214:217]
	v_fma_f32 v230, v226, v230, v230
	v_rcp_f32_e32 v230, v230
	v_mfma_f32_16x16x32_f16 v[218:221], v[18:21], v[158:161], v[218:221]
	v_fma_f32 v226, -v228, v230, v230
	v_fma_f32 v200, v200, v227, v226
	v_mfma_f32_16x16x32_f16 v[218:221], v[14:17], v[162:165], v[218:221]
	v_min_f32_e32 v226, s42, v200
	v_exp_f32_e32 v226, v226
	v_mfma_f32_16x16x32_f16 v[218:221], v[10:13], v[166:169], v[218:221]
	v_add_f32_e32 v227, 1.0, v226
	v_fma_f32 v227, v229, v227, v227
	v_mfma_f32_16x16x32_f16 v[218:221], v[26:29], v[170:173], v[218:221]
	v_rcp_f32_e32 v227, v227
	v_exp_f32_e32 v231, v214
	v_mfma_f32_16x16x32_f16 v[222:225], v[2:5], v[158:161], v[222:225]
	v_exp_f32_e32 v232, v215
	v_fma_mixlo_f16 v246, -v226, v227, v227
	v_mfma_f32_16x16x32_f16 v[222:225], v[6:9], v[162:165], v[222:225]
	v_min_f32_e32 v233, s42, v216
	v_exp_f32_e32 v234, v217
	v_mfma_f32_16x16x32_f16 v[222:225], v[22:25], v[166:169], v[222:225]
	v_exp_f32_e32 v236, v218
	v_exp_f32_e32 v233, v233
	v_mfma_f32_16x16x32_f16 v[222:225], v[30:33], v[170:173], v[222:225]
	v_add_f32_e32 v232, 1.0, v232
	v_exp_f32_e32 v227, v219
	v_fma_f32 v235, v233, s41, s41
	v_rcp_f32_e32 v232, v232
	v_min_f32_e32 v228, s42, v220
	v_fma_f32 v235, v231, v235, v235
	v_rcp_f32_e32 v235, v235
	v_exp_f32_e32 v229, v221
	v_fma_f32 v231, -v233, v235, v235
	v_fma_f32 v201, v201, v232, v231
	v_exp_f32_e32 v228, v228
	v_min_f32_e32 v231, s42, v201
	v_exp_f32_e32 v231, v231
	v_add_f32_e32 v227, 1.0, v227
	v_add_f32_e32 v232, 1.0, v231
	v_mfma_f32_16x16x32_f16 v[146:149], v[138:141], v[158:161], v[146:149]
	v_fma_f32 v232, v234, v232, v232
	v_fma_f32 v230, v228, s41, s41
	v_rcp_f32_e32 v232, v232
	v_mfma_f32_16x16x32_f16 v[146:149], v[142:145], v[162:165], v[146:149]
	v_fma_mixhi_f16 v246, -v231, v232, v232
	v_rcp_f32_e32 v227, v227
	v_exp_f32_e32 v231, v222
	buffer_load_dwordx4 v[138:141], v189, s[16:19], s46 offen
	buffer_load_dwordx4 v[142:145], v208, s[16:19], s46 offen
	v_exp_f32_e32 v232, v223
	v_fma_f32 v230, v236, v230, v230
	v_min_f32_e32 v233, s42, v224
	s_waitcnt lgkmcnt(0)
	v_mfma_f32_16x16x32_f16 v[210:213], v[70:73], v[150:153], v[98:101]
	v_exp_f32_e32 v234, v225
	v_rcp_f32_e32 v230, v230
	v_exp_f32_e32 v233, v233
	v_mfma_f32_16x16x32_f16 v[214:217], v[74:77], v[150:153], v[102:105]
	v_add_f32_e32 v232, 1.0, v232
	v_fma_f32 v236, -v228, v230, v230
	v_fma_f32 v235, v233, s41, s41
	v_rcp_f32_e32 v232, v232
	v_fma_f32 v198, v198, v227, v236
	v_fma_f32 v235, v231, v235, v235
	v_rcp_f32_e32 v235, v235
	v_min_f32_e32 v236, s42, v198
	v_fma_f32 v231, -v233, v235, v235
	v_fma_f32 v199, v199, v232, v231
	v_exp_f32_e32 v236, v236
	v_min_f32_e32 v231, s42, v199
	v_exp_f32_e32 v231, v231
	v_add_f32_e32 v227, 1.0, v236
	v_add_f32_e32 v232, 1.0, v231
	v_fma_f32 v227, v229, v227, v227
	v_fma_f32 v232, v234, v232, v232
	v_rcp_f32_e32 v227, v227
	v_rcp_f32_e32 v232, v232
	v_fma_mixlo_f16 v247, -v236, v227, v227
	v_fma_mixhi_f16 v247, -v231, v232, v232
	ds_write_b64 v206, v[246:247] offset:8192
	v_mfma_f32_16x16x32_f16 v[210:213], v[66:69], v[154:157], v[210:213]
	v_mfma_f32_16x16x32_f16 v[214:217], v[78:81], v[154:157], v[214:217]
	v_mov_b32_e32 v241, v246
	v_mov_b32_e32 v242, v247
	buffer_load_dwordx2 v[196:197], v209, s[20:23], s45 offen
	s_add_i32 s40, s40, 1
	s_add_i32 s44, s44, 0x1000
	s_waitcnt lgkmcnt(0)
	s_barrier
	ds_read_b128 v[158:161], v252 offset:0
	ds_read_b128 v[162:165], v252 offset:1024
	ds_read_b128 v[166:169], v253 offset:2048
	ds_read_b128 v[170:173], v253 offset:3072
	v_mfma_f32_16x16x32_f16 v[218:221], v[82:85], v[150:153], v[106:109]
	v_mfma_f32_16x16x32_f16 v[222:225], v[90:93], v[150:153], v[110:113]
	v_mfma_f32_16x16x32_f16 v[218:221], v[86:89], v[154:157], v[218:221]
	v_mfma_f32_16x16x32_f16 v[222:225], v[94:97], v[154:157], v[222:225]
	s_waitcnt lgkmcnt(2)
	v_mfma_f32_16x16x32_f16 v[210:213], v[54:57], v[158:161], v[210:213]
	v_mfma_f32_16x16x32_f16 v[210:213], v[58:61], v[162:165], v[210:213]
	s_waitcnt lgkmcnt(0)
	v_mfma_f32_16x16x32_f16 v[210:213], v[62:65], v[166:169], v[210:213]
	v_mfma_f32_16x16x32_f16 v[210:213], v[50:53], v[170:173], v[210:213]
	s_waitcnt vmcnt(9)
	v_cvt_pk_f16_f32 v251, v194, v195
	ds_write_b32 v1, v251 offset:6144
	ds_read_b128 v[150:153], v186 offset:4096
	ds_read_b128 v[154:157], v186 offset:5120
	s_add_i32 s45, s45, 0x100000
	s_add_i32 s46, s46, 0x4000
	s_movk_i32 s47, 0x1000
	s_add_i32 s43, s40, -12
	s_lshl_b32 s43, s43, 12
	s_cmp_lt_u32 s40, 14
	s_cselect_b32 s43, s47, s43
	v_exp_f32_e32 v226, v210
	v_exp_f32_e32 v227, v211
	v_mfma_f32_16x16x32_f16 v[214:217], v[34:37], v[158:161], v[214:217]
	v_min_f32_e32 v228, s42, v212
	v_exp_f32_e32 v229, v213
	v_mfma_f32_16x16x32_f16 v[214:217], v[38:41], v[162:165], v[214:217]
	v_exp_f32_e32 v228, v228
	v_add_f32_e32 v227, 1.0, v227
	v_mfma_f32_16x16x32_f16 v[214:217], v[42:45], v[166:169], v[214:217]
	v_fma_f32 v230, v228, s41, s41
	v_rcp_f32_e32 v227, v227
	v_mfma_f32_16x16x32_f16 v[214:217], v[46:49], v[170:173], v[214:217]
	v_fma_f32 v230, v226, v230, v230
	v_rcp_f32_e32 v230, v230
	v_mfma_f32_16x16x32_f16 v[218:221], v[18:21], v[158:161], v[218:221]
	v_fma_f32 v226, -v228, v230, v230
	v_fma_f32 v200, v200, v227, v226
	v_mfma_f32_16x16x32_f16 v[218:221], v[14:17], v[162:165], v[218:221]
	v_min_f32_e32 v226, s42, v200
	v_exp_f32_e32 v226, v226
	v_mfma_f32_16x16x32_f16 v[218:221], v[10:13], v[166:169], v[218:221]
	v_add_f32_e32 v227, 1.0, v226
	v_fma_f32 v227, v229, v227, v227
	v_mfma_f32_16x16x32_f16 v[218:221], v[26:29], v[170:173], v[218:221]
	v_rcp_f32_e32 v227, v227
	v_exp_f32_e32 v231, v214
	v_mfma_f32_16x16x32_f16 v[222:225], v[2:5], v[158:161], v[222:225]
	v_exp_f32_e32 v232, v215
	v_fma_mixlo_f16 v246, -v226, v227, v227
	v_mfma_f32_16x16x32_f16 v[222:225], v[6:9], v[162:165], v[222:225]
	v_min_f32_e32 v233, s42, v216
	v_exp_f32_e32 v234, v217
	v_mfma_f32_16x16x32_f16 v[222:225], v[22:25], v[166:169], v[222:225]
	v_exp_f32_e32 v236, v218
	v_exp_f32_e32 v233, v233
	v_mfma_f32_16x16x32_f16 v[222:225], v[30:33], v[170:173], v[222:225]
	v_add_f32_e32 v232, 1.0, v232
	v_exp_f32_e32 v227, v219
	v_fma_f32 v235, v233, s41, s41
	v_rcp_f32_e32 v232, v232
	v_min_f32_e32 v228, s42, v220
	v_fma_f32 v235, v231, v235, v235
	v_rcp_f32_e32 v235, v235
	v_exp_f32_e32 v229, v221
	v_fma_f32 v231, -v233, v235, v235
	v_fma_f32 v201, v201, v232, v231
	v_exp_f32_e32 v228, v228
	v_min_f32_e32 v231, s42, v201
	v_exp_f32_e32 v231, v231
	v_add_f32_e32 v227, 1.0, v227
	v_add_f32_e32 v232, 1.0, v231
	v_mfma_f32_16x16x32_f16 v[146:149], v[130:133], v[158:161], v[146:149]
	v_fma_f32 v232, v234, v232, v232
	v_fma_f32 v230, v228, s41, s41
	v_rcp_f32_e32 v232, v232
	v_mfma_f32_16x16x32_f16 v[146:149], v[134:137], v[162:165], v[146:149]
	v_fma_mixhi_f16 v246, -v231, v232, v232
	v_rcp_f32_e32 v227, v227
	v_exp_f32_e32 v231, v222
	buffer_load_dwordx4 v[130:133], v189, s[16:19], s46 offen
	buffer_load_dwordx4 v[134:137], v208, s[16:19], s46 offen
	v_exp_f32_e32 v232, v223
	v_fma_f32 v230, v236, v230, v230
	v_min_f32_e32 v233, s42, v224
	s_waitcnt lgkmcnt(0)
	v_mfma_f32_16x16x32_f16 v[210:213], v[70:73], v[150:153], v[98:101]
	v_exp_f32_e32 v234, v225
	v_rcp_f32_e32 v230, v230
	v_exp_f32_e32 v233, v233
	v_mfma_f32_16x16x32_f16 v[214:217], v[74:77], v[150:153], v[102:105]
	v_add_f32_e32 v232, 1.0, v232
	v_fma_f32 v236, -v228, v230, v230
	v_fma_f32 v235, v233, s41, s41
	v_rcp_f32_e32 v232, v232
	v_fma_f32 v198, v198, v227, v236
	v_fma_f32 v235, v231, v235, v235
	v_rcp_f32_e32 v235, v235
	v_min_f32_e32 v236, s42, v198
	v_fma_f32 v231, -v233, v235, v235
	v_fma_f32 v199, v199, v232, v231
	v_exp_f32_e32 v236, v236
	v_min_f32_e32 v231, s42, v199
	v_exp_f32_e32 v231, v231
	v_add_f32_e32 v227, 1.0, v236
	v_add_f32_e32 v232, 1.0, v231
	v_fma_f32 v227, v229, v227, v227
	v_fma_f32 v232, v234, v232, v232
	v_rcp_f32_e32 v227, v227
	v_rcp_f32_e32 v232, v232
	v_fma_mixlo_f16 v247, -v236, v227, v227
	v_fma_mixhi_f16 v247, -v231, v232, v232
	ds_write_b64 v206, v[246:247] offset:12288
	v_mfma_f32_16x16x32_f16 v[210:213], v[66:69], v[154:157], v[210:213]
	v_mfma_f32_16x16x32_f16 v[214:217], v[78:81], v[154:157], v[214:217]
	v_mov_b32_e32 v243, v246
	v_mov_b32_e32 v244, v247
	buffer_load_dwordx2 v[194:195], v209, s[20:23], s45 offen
	s_add_i32 s40, s40, 1
	s_add_i32 s44, s44, 0x1000
	s_waitcnt lgkmcnt(0)
	s_barrier
	ds_read_b128 v[158:161], v252 offset:4096
	ds_read_b128 v[162:165], v252 offset:5120
	ds_read_b128 v[166:169], v253 offset:6144
	ds_read_b128 v[170:173], v253 offset:7168
	v_mfma_f32_16x16x32_f16 v[218:221], v[82:85], v[150:153], v[106:109]
	v_mfma_f32_16x16x32_f16 v[222:225], v[90:93], v[150:153], v[110:113]
	v_mfma_f32_16x16x32_f16 v[218:221], v[86:89], v[154:157], v[218:221]
	v_mfma_f32_16x16x32_f16 v[222:225], v[94:97], v[154:157], v[222:225]
	s_waitcnt lgkmcnt(2)
	v_mfma_f32_16x16x32_f16 v[210:213], v[54:57], v[158:161], v[210:213]
	v_mfma_f32_16x16x32_f16 v[210:213], v[58:61], v[162:165], v[210:213]
	s_waitcnt lgkmcnt(0)
	v_mfma_f32_16x16x32_f16 v[210:213], v[62:65], v[166:169], v[210:213]
	v_mfma_f32_16x16x32_f16 v[210:213], v[50:53], v[170:173], v[210:213]
	s_waitcnt vmcnt(9)
	v_cvt_pk_f16_f32 v251, v192, v193
	ds_write_b32 v1, v251 offset:0
	ds_read_b128 v[150:153], v186 offset:6144
	ds_read_b128 v[154:157], v186 offset:7168
	s_add_i32 s45, s45, 0x100000
	s_add_i32 s46, s46, 0x4000
	s_movk_i32 s47, 0x0
	s_add_i32 s43, s40, -12
	s_lshl_b32 s43, s43, 12
	s_cmp_lt_u32 s40, 14
	s_cselect_b32 s43, s47, s43
	v_exp_f32_e32 v226, v210
	v_exp_f32_e32 v227, v211
	v_mfma_f32_16x16x32_f16 v[214:217], v[34:37], v[158:161], v[214:217]
	v_min_f32_e32 v228, s42, v212
	v_exp_f32_e32 v229, v213
	v_mfma_f32_16x16x32_f16 v[214:217], v[38:41], v[162:165], v[214:217]
	v_exp_f32_e32 v228, v228
	v_add_f32_e32 v227, 1.0, v227
	v_mfma_f32_16x16x32_f16 v[214:217], v[42:45], v[166:169], v[214:217]
	v_fma_f32 v230, v228, s41, s41
	v_rcp_f32_e32 v227, v227
	v_mfma_f32_16x16x32_f16 v[214:217], v[46:49], v[170:173], v[214:217]
	v_fma_f32 v230, v226, v230, v230
	v_rcp_f32_e32 v230, v230
	v_mfma_f32_16x16x32_f16 v[218:221], v[18:21], v[158:161], v[218:221]
	v_fma_f32 v226, -v228, v230, v230
	v_fma_f32 v200, v200, v227, v226
	v_mfma_f32_16x16x32_f16 v[218:221], v[14:17], v[162:165], v[218:221]
	v_min_f32_e32 v226, s42, v200
	v_exp_f32_e32 v226, v226
	v_mfma_f32_16x16x32_f16 v[218:221], v[10:13], v[166:169], v[218:221]
	v_add_f32_e32 v227, 1.0, v226
	v_fma_f32 v227, v229, v227, v227
	v_mfma_f32_16x16x32_f16 v[218:221], v[26:29], v[170:173], v[218:221]
	v_rcp_f32_e32 v227, v227
	v_exp_f32_e32 v231, v214
	v_mfma_f32_16x16x32_f16 v[222:225], v[2:5], v[158:161], v[222:225]
	v_exp_f32_e32 v232, v215
	v_fma_mixlo_f16 v246, -v226, v227, v227
	v_mfma_f32_16x16x32_f16 v[222:225], v[6:9], v[162:165], v[222:225]
	v_min_f32_e32 v233, s42, v216
	v_exp_f32_e32 v234, v217
	v_mfma_f32_16x16x32_f16 v[222:225], v[22:25], v[166:169], v[222:225]
	v_exp_f32_e32 v236, v218
	v_exp_f32_e32 v233, v233
	v_mfma_f32_16x16x32_f16 v[222:225], v[30:33], v[170:173], v[222:225]
	v_add_f32_e32 v232, 1.0, v232
	v_exp_f32_e32 v227, v219
	v_fma_f32 v235, v233, s41, s41
	v_rcp_f32_e32 v232, v232
	v_min_f32_e32 v228, s42, v220
	v_fma_f32 v235, v231, v235, v235
	v_rcp_f32_e32 v235, v235
	v_exp_f32_e32 v229, v221
	v_fma_f32 v231, -v233, v235, v235
	v_fma_f32 v201, v201, v232, v231
	v_exp_f32_e32 v228, v228
	v_min_f32_e32 v231, s42, v201
	v_exp_f32_e32 v231, v231
	v_add_f32_e32 v227, 1.0, v227
	v_add_f32_e32 v232, 1.0, v231
	v_mfma_f32_16x16x32_f16 v[146:149], v[122:125], v[158:161], v[146:149]
	v_fma_f32 v232, v234, v232, v232
	v_fma_f32 v230, v228, s41, s41
	v_rcp_f32_e32 v232, v232
	v_mfma_f32_16x16x32_f16 v[146:149], v[126:129], v[162:165], v[146:149]
	v_fma_mixhi_f16 v246, -v231, v232, v232
	v_rcp_f32_e32 v227, v227
	v_exp_f32_e32 v231, v222
	buffer_load_dwordx4 v[122:125], v189, s[16:19], s46 offen
	buffer_load_dwordx4 v[126:129], v208, s[16:19], s46 offen
	v_exp_f32_e32 v232, v223
	v_fma_f32 v230, v236, v230, v230
	v_min_f32_e32 v233, s42, v224
	s_waitcnt lgkmcnt(0)
	v_mfma_f32_16x16x32_f16 v[210:213], v[70:73], v[150:153], v[98:101]
	v_exp_f32_e32 v234, v225
	v_rcp_f32_e32 v230, v230
	v_exp_f32_e32 v233, v233
	v_mfma_f32_16x16x32_f16 v[214:217], v[74:77], v[150:153], v[102:105]
	v_add_f32_e32 v232, 1.0, v232
	v_fma_f32 v236, -v228, v230, v230
	v_fma_f32 v235, v233, s41, s41
	v_rcp_f32_e32 v232, v232
	v_fma_f32 v198, v198, v227, v236
	v_fma_f32 v235, v231, v235, v235
	v_rcp_f32_e32 v235, v235
	v_min_f32_e32 v236, s42, v198
	v_fma_f32 v231, -v233, v235, v235
	v_fma_f32 v199, v199, v232, v231
	v_exp_f32_e32 v236, v236
	v_min_f32_e32 v231, s42, v199
	v_exp_f32_e32 v231, v231
	v_add_f32_e32 v227, 1.0, v236
	v_add_f32_e32 v232, 1.0, v231
	v_fma_f32 v227, v229, v227, v227
	v_fma_f32 v232, v234, v232, v232
	v_rcp_f32_e32 v227, v227
	v_rcp_f32_e32 v232, v232
	v_fma_mixlo_f16 v247, -v236, v227, v227
	v_fma_mixhi_f16 v247, -v231, v232, v232
	ds_write_b64 v206, v[246:247] offset:8192
	v_mfma_f32_16x16x32_f16 v[210:213], v[66:69], v[154:157], v[210:213]
	v_mfma_f32_16x16x32_f16 v[214:217], v[78:81], v[154:157], v[214:217]
	v_mov_b32_e32 v245, v246
	v_mov_b32_e32 v187, v247
	buffer_load_dwordx2 v[192:193], v209, s[20:23], s45 offen
	s_add_i32 s40, s40, 1
	s_add_i32 s44, s44, 0x1000
	s_waitcnt lgkmcnt(0)
	s_barrier
	ds_read_b128 v[158:161], v252 offset:0
	ds_read_b128 v[162:165], v252 offset:1024
	ds_read_b128 v[166:169], v253 offset:2048
	ds_read_b128 v[170:173], v253 offset:3072
	v_mfma_f32_16x16x32_f16 v[218:221], v[82:85], v[150:153], v[106:109]
	v_mfma_f32_16x16x32_f16 v[222:225], v[90:93], v[150:153], v[110:113]
	v_mfma_f32_16x16x32_f16 v[218:221], v[86:89], v[154:157], v[218:221]
	v_mfma_f32_16x16x32_f16 v[222:225], v[94:97], v[154:157], v[222:225]
	s_waitcnt lgkmcnt(2)
	v_mfma_f32_16x16x32_f16 v[210:213], v[54:57], v[158:161], v[210:213]
	v_mfma_f32_16x16x32_f16 v[210:213], v[58:61], v[162:165], v[210:213]
	s_waitcnt lgkmcnt(0)
	v_mfma_f32_16x16x32_f16 v[210:213], v[62:65], v[166:169], v[210:213]
	v_mfma_f32_16x16x32_f16 v[210:213], v[50:53], v[170:173], v[210:213]
	s_waitcnt vmcnt(9)
	v_cvt_pk_f16_f32 v251, v190, v191
	ds_write_b32 v1, v251 offset:2048
	ds_read_b128 v[150:153], v186 offset:0
	ds_read_b128 v[154:157], v186 offset:1024
	s_add_i32 s45, s45, 0x100000
	s_add_i32 s46, s46, 0x4000
	s_movk_i32 s47, 0x1000
	s_add_i32 s43, s40, -12
	s_lshl_b32 s43, s43, 12
	s_cmp_lt_u32 s40, 14
	s_cselect_b32 s43, s47, s43
	v_exp_f32_e32 v226, v210
	v_exp_f32_e32 v227, v211
	v_mfma_f32_16x16x32_f16 v[214:217], v[34:37], v[158:161], v[214:217]
	v_min_f32_e32 v228, s42, v212
	v_exp_f32_e32 v229, v213
	v_mfma_f32_16x16x32_f16 v[214:217], v[38:41], v[162:165], v[214:217]
	v_exp_f32_e32 v228, v228
	v_add_f32_e32 v227, 1.0, v227
	v_mfma_f32_16x16x32_f16 v[214:217], v[42:45], v[166:169], v[214:217]
	v_fma_f32 v230, v228, s41, s41
	v_rcp_f32_e32 v227, v227
	v_mfma_f32_16x16x32_f16 v[214:217], v[46:49], v[170:173], v[214:217]
	v_fma_f32 v230, v226, v230, v230
	v_rcp_f32_e32 v230, v230
	v_mfma_f32_16x16x32_f16 v[218:221], v[18:21], v[158:161], v[218:221]
	v_fma_f32 v226, -v228, v230, v230
	v_fma_f32 v200, v200, v227, v226
	v_mfma_f32_16x16x32_f16 v[218:221], v[14:17], v[162:165], v[218:221]
	v_min_f32_e32 v226, s42, v200
	v_exp_f32_e32 v226, v226
	v_mfma_f32_16x16x32_f16 v[218:221], v[10:13], v[166:169], v[218:221]
	v_add_f32_e32 v227, 1.0, v226
	v_fma_f32 v227, v229, v227, v227
	v_mfma_f32_16x16x32_f16 v[218:221], v[26:29], v[170:173], v[218:221]
	v_rcp_f32_e32 v227, v227
	v_exp_f32_e32 v231, v214
	v_mfma_f32_16x16x32_f16 v[222:225], v[2:5], v[158:161], v[222:225]
	v_exp_f32_e32 v232, v215
	v_fma_mixlo_f16 v246, -v226, v227, v227
	v_mfma_f32_16x16x32_f16 v[222:225], v[6:9], v[162:165], v[222:225]
	v_min_f32_e32 v233, s42, v216
	v_exp_f32_e32 v234, v217
	v_mfma_f32_16x16x32_f16 v[222:225], v[22:25], v[166:169], v[222:225]
	v_exp_f32_e32 v236, v218
	v_exp_f32_e32 v233, v233
	v_mfma_f32_16x16x32_f16 v[222:225], v[30:33], v[170:173], v[222:225]
	v_add_f32_e32 v232, 1.0, v232
	v_exp_f32_e32 v227, v219
	v_fma_f32 v235, v233, s41, s41
	v_rcp_f32_e32 v232, v232
	v_min_f32_e32 v228, s42, v220
	v_fma_f32 v235, v231, v235, v235
	v_rcp_f32_e32 v235, v235
	v_exp_f32_e32 v229, v221
	v_fma_f32 v231, -v233, v235, v235
	v_fma_f32 v201, v201, v232, v231
	v_exp_f32_e32 v228, v228
	v_min_f32_e32 v231, s42, v201
	v_exp_f32_e32 v231, v231
	v_add_f32_e32 v227, 1.0, v227
	v_add_f32_e32 v232, 1.0, v231
	v_mfma_f32_16x16x32_f16 v[146:149], v[114:117], v[158:161], v[146:149]
	v_fma_f32 v232, v234, v232, v232
	v_fma_f32 v230, v228, s41, s41
	v_rcp_f32_e32 v232, v232
	v_mfma_f32_16x16x32_f16 v[146:149], v[118:121], v[162:165], v[146:149]
	v_fma_mixhi_f16 v246, -v231, v232, v232
	v_rcp_f32_e32 v227, v227
	v_exp_f32_e32 v231, v222
	buffer_load_dwordx4 v[114:117], v189, s[16:19], s46 offen
	buffer_load_dwordx4 v[118:121], v208, s[16:19], s46 offen
	v_exp_f32_e32 v232, v223
	v_fma_f32 v230, v236, v230, v230
	v_min_f32_e32 v233, s42, v224
	s_waitcnt lgkmcnt(0)
	v_mfma_f32_16x16x32_f16 v[210:213], v[70:73], v[150:153], v[98:101]
	v_exp_f32_e32 v234, v225
	v_rcp_f32_e32 v230, v230
	v_exp_f32_e32 v233, v233
	v_mfma_f32_16x16x32_f16 v[214:217], v[74:77], v[150:153], v[102:105]
	v_add_f32_e32 v232, 1.0, v232
	v_fma_f32 v236, -v228, v230, v230
	v_fma_f32 v235, v233, s41, s41
	v_rcp_f32_e32 v232, v232
	v_fma_f32 v198, v198, v227, v236
	v_fma_f32 v235, v231, v235, v235
	v_rcp_f32_e32 v235, v235
	v_min_f32_e32 v236, s42, v198
	v_fma_f32 v231, -v233, v235, v235
	v_fma_f32 v199, v199, v232, v231
	v_exp_f32_e32 v236, v236
	v_min_f32_e32 v231, s42, v199
	v_exp_f32_e32 v231, v231
	v_add_f32_e32 v227, 1.0, v236
	v_add_f32_e32 v232, 1.0, v231
	v_fma_f32 v227, v229, v227, v227
	v_fma_f32 v232, v234, v232, v232
	v_rcp_f32_e32 v227, v227
	v_rcp_f32_e32 v232, v232
	v_fma_mixlo_f16 v247, -v236, v227, v227
	v_fma_mixhi_f16 v247, -v231, v232, v232
	ds_write_b64 v206, v[246:247] offset:12288
	v_mfma_f32_16x16x32_f16 v[210:213], v[66:69], v[154:157], v[210:213]
	v_mfma_f32_16x16x32_f16 v[214:217], v[78:81], v[154:157], v[214:217]
	v_mov_b32_e32 v188, v246
	v_mov_b32_e32 v202, v247
	buffer_load_dwordx2 v[190:191], v209, s[20:23], s45 offen
	s_add_i32 s40, s40, 1
	s_add_i32 s44, s44, 0x1000
	s_waitcnt lgkmcnt(0)
	s_barrier
	ds_read_b128 v[158:161], v252 offset:4096
	ds_read_b128 v[162:165], v252 offset:5120
	ds_read_b128 v[166:169], v253 offset:6144
	ds_read_b128 v[170:173], v253 offset:7168
	v_mfma_f32_16x16x32_f16 v[218:221], v[82:85], v[150:153], v[106:109]
	v_mfma_f32_16x16x32_f16 v[222:225], v[90:93], v[150:153], v[110:113]
	v_mfma_f32_16x16x32_f16 v[218:221], v[86:89], v[154:157], v[218:221]
	v_mfma_f32_16x16x32_f16 v[222:225], v[94:97], v[154:157], v[222:225]
	s_waitcnt lgkmcnt(2)
	v_mfma_f32_16x16x32_f16 v[210:213], v[54:57], v[158:161], v[210:213]
	v_mfma_f32_16x16x32_f16 v[210:213], v[58:61], v[162:165], v[210:213]
	s_waitcnt lgkmcnt(0)
	v_mfma_f32_16x16x32_f16 v[210:213], v[62:65], v[166:169], v[210:213]
	v_mfma_f32_16x16x32_f16 v[210:213], v[50:53], v[170:173], v[210:213]
	s_waitcnt vmcnt(9)
	v_cvt_pk_f16_f32 v251, v196, v197
	ds_write_b32 v1, v251 offset:4096
	ds_read_b128 v[150:153], v186 offset:2048
	ds_read_b128 v[154:157], v186 offset:3072
	s_add_i32 s45, s45, 0x100000
	s_add_i32 s46, s46, 0x4000
	s_movk_i32 s47, 0x0
	s_add_i32 s43, s40, -12
	s_lshl_b32 s43, s43, 12
	s_cmp_lt_u32 s40, 14
	s_cselect_b32 s43, s47, s43
	v_exp_f32_e32 v226, v210
	v_exp_f32_e32 v227, v211
	v_mfma_f32_16x16x32_f16 v[214:217], v[34:37], v[158:161], v[214:217]
	v_min_f32_e32 v228, s42, v212
	v_exp_f32_e32 v229, v213
	v_mfma_f32_16x16x32_f16 v[214:217], v[38:41], v[162:165], v[214:217]
	v_exp_f32_e32 v228, v228
	v_add_f32_e32 v227, 1.0, v227
	v_mfma_f32_16x16x32_f16 v[214:217], v[42:45], v[166:169], v[214:217]
	v_fma_f32 v230, v228, s41, s41
	v_rcp_f32_e32 v227, v227
	v_mfma_f32_16x16x32_f16 v[214:217], v[46:49], v[170:173], v[214:217]
	v_fma_f32 v230, v226, v230, v230
	v_rcp_f32_e32 v230, v230
	v_mfma_f32_16x16x32_f16 v[218:221], v[18:21], v[158:161], v[218:221]
	v_fma_f32 v226, -v228, v230, v230
	v_fma_f32 v200, v200, v227, v226
	v_mfma_f32_16x16x32_f16 v[218:221], v[14:17], v[162:165], v[218:221]
	v_min_f32_e32 v226, s42, v200
	v_exp_f32_e32 v226, v226
	v_mfma_f32_16x16x32_f16 v[218:221], v[10:13], v[166:169], v[218:221]
	v_add_f32_e32 v227, 1.0, v226
	v_fma_f32 v227, v229, v227, v227
	v_mfma_f32_16x16x32_f16 v[218:221], v[26:29], v[170:173], v[218:221]
	v_rcp_f32_e32 v227, v227
	v_exp_f32_e32 v231, v214
	v_mfma_f32_16x16x32_f16 v[222:225], v[2:5], v[158:161], v[222:225]
	v_exp_f32_e32 v232, v215
	v_fma_mixlo_f16 v246, -v226, v227, v227
	v_mfma_f32_16x16x32_f16 v[222:225], v[6:9], v[162:165], v[222:225]
	v_min_f32_e32 v233, s42, v216
	v_exp_f32_e32 v234, v217
	v_mfma_f32_16x16x32_f16 v[222:225], v[22:25], v[166:169], v[222:225]
	v_exp_f32_e32 v236, v218
	v_exp_f32_e32 v233, v233
	v_mfma_f32_16x16x32_f16 v[222:225], v[30:33], v[170:173], v[222:225]
	v_add_f32_e32 v232, 1.0, v232
	v_exp_f32_e32 v227, v219
	v_fma_f32 v235, v233, s41, s41
	v_rcp_f32_e32 v232, v232
	v_min_f32_e32 v228, s42, v220
	v_fma_f32 v235, v231, v235, v235
	v_rcp_f32_e32 v235, v235
	v_exp_f32_e32 v229, v221
	v_fma_f32 v231, -v233, v235, v235
	v_fma_f32 v201, v201, v232, v231
	v_exp_f32_e32 v228, v228
	v_min_f32_e32 v231, s42, v201
	v_exp_f32_e32 v231, v231
	v_add_f32_e32 v227, 1.0, v227
	v_add_f32_e32 v232, 1.0, v231
	v_mfma_f32_16x16x32_f16 v[146:149], v[138:141], v[158:161], v[146:149]
	v_fma_f32 v232, v234, v232, v232
	v_fma_f32 v230, v228, s41, s41
	v_rcp_f32_e32 v232, v232
	v_mfma_f32_16x16x32_f16 v[146:149], v[142:145], v[162:165], v[146:149]
	v_fma_mixhi_f16 v246, -v231, v232, v232
	v_rcp_f32_e32 v227, v227
	v_exp_f32_e32 v231, v222
	buffer_load_dwordx4 v[138:141], v189, s[16:19], s46 offen
	buffer_load_dwordx4 v[142:145], v208, s[16:19], s46 offen
	v_exp_f32_e32 v232, v223
	v_fma_f32 v230, v236, v230, v230
	v_min_f32_e32 v233, s42, v224
	s_waitcnt lgkmcnt(0)
	v_mfma_f32_16x16x32_f16 v[210:213], v[70:73], v[150:153], v[98:101]
	v_exp_f32_e32 v234, v225
	v_rcp_f32_e32 v230, v230
	v_exp_f32_e32 v233, v233
	v_mfma_f32_16x16x32_f16 v[214:217], v[74:77], v[150:153], v[102:105]
	v_add_f32_e32 v232, 1.0, v232
	v_fma_f32 v236, -v228, v230, v230
	v_fma_f32 v235, v233, s41, s41
	v_rcp_f32_e32 v232, v232
	v_fma_f32 v198, v198, v227, v236
	v_fma_f32 v235, v231, v235, v235
	v_rcp_f32_e32 v235, v235
	v_min_f32_e32 v236, s42, v198
	v_fma_f32 v231, -v233, v235, v235
	v_fma_f32 v199, v199, v232, v231
	v_exp_f32_e32 v236, v236
	v_min_f32_e32 v231, s42, v199
	v_exp_f32_e32 v231, v231
	v_add_f32_e32 v227, 1.0, v236
	v_add_f32_e32 v232, 1.0, v231
	v_fma_f32 v227, v229, v227, v227
	v_fma_f32 v232, v234, v232, v232
	v_rcp_f32_e32 v227, v227
	v_rcp_f32_e32 v232, v232
	v_fma_mixlo_f16 v247, -v236, v227, v227
	v_fma_mixhi_f16 v247, -v231, v232, v232
	ds_write_b64 v206, v[246:247] offset:8192
	v_mfma_f32_16x16x32_f16 v[210:213], v[66:69], v[154:157], v[210:213]
	v_mfma_f32_16x16x32_f16 v[214:217], v[78:81], v[154:157], v[214:217]
	v_mov_b32_e32 v203, v246
	v_mov_b32_e32 v204, v247
	buffer_load_dwordx2 v[196:197], v209, s[20:23], s45 offen
	s_add_i32 s40, s40, 1
	s_add_i32 s44, s44, 0x1000
	s_waitcnt lgkmcnt(0)
	s_barrier
	ds_read_b128 v[158:161], v252 offset:0
	ds_read_b128 v[162:165], v252 offset:1024
	ds_read_b128 v[166:169], v253 offset:2048
	ds_read_b128 v[170:173], v253 offset:3072
	v_mfma_f32_16x16x32_f16 v[218:221], v[82:85], v[150:153], v[106:109]
	v_mfma_f32_16x16x32_f16 v[222:225], v[90:93], v[150:153], v[110:113]
	v_mfma_f32_16x16x32_f16 v[218:221], v[86:89], v[154:157], v[218:221]
	v_mfma_f32_16x16x32_f16 v[222:225], v[94:97], v[154:157], v[222:225]
	s_waitcnt lgkmcnt(2)
	v_mfma_f32_16x16x32_f16 v[210:213], v[54:57], v[158:161], v[210:213]
	v_mfma_f32_16x16x32_f16 v[210:213], v[58:61], v[162:165], v[210:213]
	s_waitcnt lgkmcnt(0)
	v_mfma_f32_16x16x32_f16 v[210:213], v[62:65], v[166:169], v[210:213]
	v_mfma_f32_16x16x32_f16 v[210:213], v[50:53], v[170:173], v[210:213]
	s_waitcnt vmcnt(9)
	v_cvt_pk_f16_f32 v251, v194, v195
	ds_write_b32 v1, v251 offset:6144
	ds_read_b128 v[150:153], v186 offset:4096
	ds_read_b128 v[154:157], v186 offset:5120
	s_add_i32 s45, s45, 0x100000
	s_add_i32 s46, s46, 0x4000
	s_movk_i32 s47, 0x1000
	s_add_i32 s43, s40, -12
	s_lshl_b32 s43, s43, 12
	s_cmp_lt_u32 s40, 14
	s_cselect_b32 s43, s47, s43
	v_exp_f32_e32 v226, v210
	v_exp_f32_e32 v227, v211
	v_mfma_f32_16x16x32_f16 v[214:217], v[34:37], v[158:161], v[214:217]
	v_min_f32_e32 v228, s42, v212
	v_exp_f32_e32 v229, v213
	v_mfma_f32_16x16x32_f16 v[214:217], v[38:41], v[162:165], v[214:217]
	v_exp_f32_e32 v228, v228
	v_add_f32_e32 v227, 1.0, v227
	v_mfma_f32_16x16x32_f16 v[214:217], v[42:45], v[166:169], v[214:217]
	v_fma_f32 v230, v228, s41, s41
	v_rcp_f32_e32 v227, v227
	v_mfma_f32_16x16x32_f16 v[214:217], v[46:49], v[170:173], v[214:217]
	v_fma_f32 v230, v226, v230, v230
	v_rcp_f32_e32 v230, v230
	v_mfma_f32_16x16x32_f16 v[218:221], v[18:21], v[158:161], v[218:221]
	v_fma_f32 v226, -v228, v230, v230
	v_fma_f32 v200, v200, v227, v226
	v_mfma_f32_16x16x32_f16 v[218:221], v[14:17], v[162:165], v[218:221]
	v_min_f32_e32 v226, s42, v200
	v_exp_f32_e32 v226, v226
	v_mfma_f32_16x16x32_f16 v[218:221], v[10:13], v[166:169], v[218:221]
	v_add_f32_e32 v227, 1.0, v226
	v_fma_f32 v227, v229, v227, v227
	v_mfma_f32_16x16x32_f16 v[218:221], v[26:29], v[170:173], v[218:221]
	v_rcp_f32_e32 v227, v227
	v_exp_f32_e32 v231, v214
	v_mfma_f32_16x16x32_f16 v[222:225], v[2:5], v[158:161], v[222:225]
	v_exp_f32_e32 v232, v215
	v_fma_mixlo_f16 v246, -v226, v227, v227
	v_mfma_f32_16x16x32_f16 v[222:225], v[6:9], v[162:165], v[222:225]
	v_min_f32_e32 v233, s42, v216
	v_exp_f32_e32 v234, v217
	v_mfma_f32_16x16x32_f16 v[222:225], v[22:25], v[166:169], v[222:225]
	v_exp_f32_e32 v236, v218
	v_exp_f32_e32 v233, v233
	v_mfma_f32_16x16x32_f16 v[222:225], v[30:33], v[170:173], v[222:225]
	v_add_f32_e32 v232, 1.0, v232
	v_exp_f32_e32 v227, v219
	v_fma_f32 v235, v233, s41, s41
	v_rcp_f32_e32 v232, v232
	v_min_f32_e32 v228, s42, v220
	v_fma_f32 v235, v231, v235, v235
	v_rcp_f32_e32 v235, v235
	v_exp_f32_e32 v229, v221
	v_fma_f32 v231, -v233, v235, v235
	v_fma_f32 v201, v201, v232, v231
	v_exp_f32_e32 v228, v228
	v_min_f32_e32 v231, s42, v201
	v_exp_f32_e32 v231, v231
	v_add_f32_e32 v227, 1.0, v227
	v_add_f32_e32 v232, 1.0, v231
	v_mfma_f32_16x16x32_f16 v[146:149], v[130:133], v[158:161], v[146:149]
	v_fma_f32 v232, v234, v232, v232
	v_fma_f32 v230, v228, s41, s41
	v_rcp_f32_e32 v232, v232
	v_mfma_f32_16x16x32_f16 v[146:149], v[134:137], v[162:165], v[146:149]
	v_fma_mixhi_f16 v246, -v231, v232, v232
	v_rcp_f32_e32 v227, v227
	v_exp_f32_e32 v231, v222
	buffer_load_dwordx4 v[130:133], v189, s[16:19], s46 offen
	buffer_load_dwordx4 v[134:137], v208, s[16:19], s46 offen
	v_exp_f32_e32 v232, v223
	v_fma_f32 v230, v236, v230, v230
	v_min_f32_e32 v233, s42, v224
	s_waitcnt lgkmcnt(0)
	v_mfma_f32_16x16x32_f16 v[210:213], v[70:73], v[150:153], v[98:101]
	v_exp_f32_e32 v234, v225
	v_rcp_f32_e32 v230, v230
	v_exp_f32_e32 v233, v233
	v_mfma_f32_16x16x32_f16 v[214:217], v[74:77], v[150:153], v[102:105]
	v_add_f32_e32 v232, 1.0, v232
	v_fma_f32 v236, -v228, v230, v230
	v_fma_f32 v235, v233, s41, s41
	v_rcp_f32_e32 v232, v232
	v_fma_f32 v198, v198, v227, v236
	v_fma_f32 v235, v231, v235, v235
	v_rcp_f32_e32 v235, v235
	v_min_f32_e32 v236, s42, v198
	v_fma_f32 v231, -v233, v235, v235
	v_fma_f32 v199, v199, v232, v231
	v_exp_f32_e32 v236, v236
	v_min_f32_e32 v231, s42, v199
	v_exp_f32_e32 v231, v231
	v_add_f32_e32 v227, 1.0, v236
	v_add_f32_e32 v232, 1.0, v231
	v_fma_f32 v227, v229, v227, v227
	v_fma_f32 v232, v234, v232, v232
	v_rcp_f32_e32 v227, v227
	v_rcp_f32_e32 v232, v232
	v_fma_mixlo_f16 v247, -v236, v227, v227
	v_fma_mixhi_f16 v247, -v231, v232, v232
	ds_write_b64 v206, v[246:247] offset:12288
	v_mfma_f32_16x16x32_f16 v[210:213], v[66:69], v[154:157], v[210:213]
	v_mfma_f32_16x16x32_f16 v[214:217], v[78:81], v[154:157], v[214:217]
	v_mov_b32_e32 v205, v246
	v_mov_b32_e32 v207, v247
	buffer_load_dwordx2 v[194:195], v209, s[20:23], s45 offen
	s_add_i32 s40, s40, 1
	s_add_i32 s44, s44, 0x1000
	s_waitcnt lgkmcnt(0)
	s_barrier
	v_add_u32_e32 v250, 0x1000, v206
	v_add_u32_e32 v248, 0x1000, v252
	v_add_u32_e32 v249, 0x1000, v253
	s_mov_b32 s45, 0xc00000
	s_mov_b32 s46, 0x30000
.Lmy_loopb:
	ds_read_b128 v[158:161], v248 offset:0
	ds_read_b128 v[162:165], v248 offset:1024
	ds_read_b128 v[166:169], v249 offset:2048
	ds_read_b128 v[170:173], v249 offset:3072
	v_mfma_f32_16x16x32_f16 v[218:221], v[82:85], v[150:153], v[106:109]
	v_mfma_f32_16x16x32_f16 v[222:225], v[90:93], v[150:153], v[110:113]
	v_mfma_f32_16x16x32_f16 v[218:221], v[86:89], v[154:157], v[218:221]
	v_mfma_f32_16x16x32_f16 v[222:225], v[94:97], v[154:157], v[222:225]
	s_waitcnt lgkmcnt(2)
	v_mfma_f32_16x16x32_f16 v[210:213], v[54:57], v[158:161], v[210:213]
	v_mfma_f32_16x16x32_f16 v[210:213], v[58:61], v[162:165], v[210:213]
	s_waitcnt lgkmcnt(0)
	v_mfma_f32_16x16x32_f16 v[210:213], v[62:65], v[166:169], v[210:213]
	v_mfma_f32_16x16x32_f16 v[210:213], v[50:53], v[170:173], v[210:213]
	s_waitcnt vmcnt(9)
	v_cvt_pk_f16_f32 v251, v192, v193
	ds_write_b32 v1, v251 offset:0
	ds_read_b128 v[150:153], v186 offset:6144
	ds_read_b128 v[154:157], v186 offset:7168
	v_add_u32_e32 v250, 0x1000, v250
	v_add_u32_e32 v248, 0x1000, v248
	v_add_u32_e32 v249, 0x1000, v249
	v_exp_f32_e32 v226, v210
	v_exp_f32_e32 v227, v211
	v_mfma_f32_16x16x32_f16 v[214:217], v[34:37], v[158:161], v[214:217]
	v_min_f32_e32 v228, s42, v212
	v_exp_f32_e32 v229, v213
	v_mfma_f32_16x16x32_f16 v[214:217], v[38:41], v[162:165], v[214:217]
	v_exp_f32_e32 v228, v228
	v_add_f32_e32 v227, 1.0, v227
	v_mfma_f32_16x16x32_f16 v[214:217], v[42:45], v[166:169], v[214:217]
	v_fma_f32 v230, v228, s41, s41
	v_rcp_f32_e32 v227, v227
	v_mfma_f32_16x16x32_f16 v[214:217], v[46:49], v[170:173], v[214:217]
	v_fma_f32 v230, v226, v230, v230
	v_rcp_f32_e32 v230, v230
	v_mfma_f32_16x16x32_f16 v[218:221], v[18:21], v[158:161], v[218:221]
	v_fma_f32 v226, -v228, v230, v230
	v_fma_f32 v200, v200, v227, v226
	v_mfma_f32_16x16x32_f16 v[218:221], v[14:17], v[162:165], v[218:221]
	v_min_f32_e32 v226, s42, v200
	v_exp_f32_e32 v226, v226
	v_mfma_f32_16x16x32_f16 v[218:221], v[10:13], v[166:169], v[218:221]
	v_add_f32_e32 v227, 1.0, v226
	v_fma_f32 v227, v229, v227, v227
	v_mfma_f32_16x16x32_f16 v[218:221], v[26:29], v[170:173], v[218:221]
	v_rcp_f32_e32 v227, v227
	v_exp_f32_e32 v231, v214
	v_mfma_f32_16x16x32_f16 v[222:225], v[2:5], v[158:161], v[222:225]
	v_exp_f32_e32 v232, v215
	v_fma_mixlo_f16 v246, -v226, v227, v227
	v_mfma_f32_16x16x32_f16 v[222:225], v[6:9], v[162:165], v[222:225]
	v_min_f32_e32 v233, s42, v216
	v_exp_f32_e32 v234, v217
	v_mfma_f32_16x16x32_f16 v[222:225], v[22:25], v[166:169], v[222:225]
	v_exp_f32_e32 v236, v218
	v_exp_f32_e32 v233, v233
	v_mfma_f32_16x16x32_f16 v[222:225], v[30:33], v[170:173], v[222:225]
	v_add_f32_e32 v232, 1.0, v232
	v_exp_f32_e32 v227, v219
	v_fma_f32 v235, v233, s41, s41
	v_rcp_f32_e32 v232, v232
	v_min_f32_e32 v228, s42, v220
	v_fma_f32 v235, v231, v235, v235
	v_rcp_f32_e32 v235, v235
	v_exp_f32_e32 v229, v221
	v_fma_f32 v231, -v233, v235, v235
	v_fma_f32 v201, v201, v232, v231
	v_exp_f32_e32 v228, v228
	v_min_f32_e32 v231, s42, v201
	v_exp_f32_e32 v231, v231
	v_add_f32_e32 v227, 1.0, v227
	v_add_f32_e32 v232, 1.0, v231
	v_mfma_f32_16x16x32_f16 v[146:149], v[122:125], v[158:161], v[146:149]
	v_fma_f32 v232, v234, v232, v232
	v_fma_f32 v230, v228, s41, s41
	v_rcp_f32_e32 v232, v232
	v_mfma_f32_16x16x32_f16 v[146:149], v[126:129], v[162:165], v[146:149]
	v_fma_mixhi_f16 v246, -v231, v232, v232
	v_rcp_f32_e32 v227, v227
	v_exp_f32_e32 v231, v222
	buffer_load_dwordx4 v[122:125], v189, s[76:79], s46 offen
	buffer_load_dwordx4 v[126:129], v208, s[76:79], s46 offen
	v_exp_f32_e32 v232, v223
	v_fma_f32 v230, v236, v230, v230
	v_min_f32_e32 v233, s42, v224
	s_waitcnt lgkmcnt(0)
	v_mfma_f32_16x16x32_f16 v[210:213], v[70:73], v[150:153], v[98:101]
	v_exp_f32_e32 v234, v225
	v_rcp_f32_e32 v230, v230
	v_exp_f32_e32 v233, v233
	v_mfma_f32_16x16x32_f16 v[214:217], v[74:77], v[150:153], v[102:105]
	v_add_f32_e32 v232, 1.0, v232
	v_fma_f32 v236, -v228, v230, v230
	v_fma_f32 v235, v233, s41, s41
	v_rcp_f32_e32 v232, v232
	v_fma_f32 v198, v198, v227, v236
	v_fma_f32 v235, v231, v235, v235
	v_rcp_f32_e32 v235, v235
	v_min_f32_e32 v236, s42, v198
	v_fma_f32 v231, -v233, v235, v235
	v_fma_f32 v199, v199, v232, v231
	v_exp_f32_e32 v236, v236
	v_min_f32_e32 v231, s42, v199
	v_exp_f32_e32 v231, v231
	v_add_f32_e32 v227, 1.0, v236
	v_add_f32_e32 v232, 1.0, v231
	v_fma_f32 v227, v229, v227, v227
	v_fma_f32 v232, v234, v232, v232
	v_rcp_f32_e32 v227, v227
	v_rcp_f32_e32 v232, v232
	v_fma_mixlo_f16 v247, -v236, v227, v227
	v_fma_mixhi_f16 v247, -v231, v232, v232
	ds_write_b64 v250, v[246:247] offset:8192
	v_mfma_f32_16x16x32_f16 v[210:213], v[66:69], v[154:157], v[210:213]
	v_mfma_f32_16x16x32_f16 v[214:217], v[78:81], v[154:157], v[214:217]
	buffer_load_dwordx2 v[192:193], v209, s[56:59], s45 offen
	s_waitcnt lgkmcnt(0)
	s_barrier
	ds_read_b128 v[158:161], v248 offset:0
	ds_read_b128 v[162:165], v248 offset:1024
	ds_read_b128 v[166:169], v249 offset:2048
	ds_read_b128 v[170:173], v249 offset:3072
	v_mfma_f32_16x16x32_f16 v[218:221], v[82:85], v[150:153], v[106:109]
	v_mfma_f32_16x16x32_f16 v[222:225], v[90:93], v[150:153], v[110:113]
	v_mfma_f32_16x16x32_f16 v[218:221], v[86:89], v[154:157], v[218:221]
	v_mfma_f32_16x16x32_f16 v[222:225], v[94:97], v[154:157], v[222:225]
	s_waitcnt lgkmcnt(2)
	v_mfma_f32_16x16x32_f16 v[210:213], v[54:57], v[158:161], v[210:213]
	v_mfma_f32_16x16x32_f16 v[210:213], v[58:61], v[162:165], v[210:213]
	s_waitcnt lgkmcnt(0)
	v_mfma_f32_16x16x32_f16 v[210:213], v[62:65], v[166:169], v[210:213]
	v_mfma_f32_16x16x32_f16 v[210:213], v[50:53], v[170:173], v[210:213]
	s_waitcnt vmcnt(9)
	v_cvt_pk_f16_f32 v251, v190, v191
	ds_write_b32 v1, v251 offset:2048
	ds_read_b128 v[150:153], v186 offset:0
	ds_read_b128 v[154:157], v186 offset:1024
	v_add_u32_e32 v250, 0x1000, v250
	v_add_u32_e32 v248, 0x1000, v248
	v_add_u32_e32 v249, 0x1000, v249
	v_exp_f32_e32 v226, v210
	v_exp_f32_e32 v227, v211
	v_mfma_f32_16x16x32_f16 v[214:217], v[34:37], v[158:161], v[214:217]
	v_min_f32_e32 v228, s42, v212
	v_exp_f32_e32 v229, v213
	v_mfma_f32_16x16x32_f16 v[214:217], v[38:41], v[162:165], v[214:217]
	v_exp_f32_e32 v228, v228
	v_add_f32_e32 v227, 1.0, v227
	v_mfma_f32_16x16x32_f16 v[214:217], v[42:45], v[166:169], v[214:217]
	v_fma_f32 v230, v228, s41, s41
	v_rcp_f32_e32 v227, v227
	v_mfma_f32_16x16x32_f16 v[214:217], v[46:49], v[170:173], v[214:217]
	v_fma_f32 v230, v226, v230, v230
	v_rcp_f32_e32 v230, v230
	v_mfma_f32_16x16x32_f16 v[218:221], v[18:21], v[158:161], v[218:221]
	v_fma_f32 v226, -v228, v230, v230
	v_fma_f32 v200, v200, v227, v226
	v_mfma_f32_16x16x32_f16 v[218:221], v[14:17], v[162:165], v[218:221]
	v_min_f32_e32 v226, s42, v200
	v_exp_f32_e32 v226, v226
	v_mfma_f32_16x16x32_f16 v[218:221], v[10:13], v[166:169], v[218:221]
	v_add_f32_e32 v227, 1.0, v226
	v_fma_f32 v227, v229, v227, v227
	v_mfma_f32_16x16x32_f16 v[218:221], v[26:29], v[170:173], v[218:221]
	v_rcp_f32_e32 v227, v227
	v_exp_f32_e32 v231, v214
	v_mfma_f32_16x16x32_f16 v[222:225], v[2:5], v[158:161], v[222:225]
	v_exp_f32_e32 v232, v215
	v_fma_mixlo_f16 v246, -v226, v227, v227
	v_mfma_f32_16x16x32_f16 v[222:225], v[6:9], v[162:165], v[222:225]
	v_min_f32_e32 v233, s42, v216
	v_exp_f32_e32 v234, v217
	v_mfma_f32_16x16x32_f16 v[222:225], v[22:25], v[166:169], v[222:225]
	v_exp_f32_e32 v236, v218
	v_exp_f32_e32 v233, v233
	v_mfma_f32_16x16x32_f16 v[222:225], v[30:33], v[170:173], v[222:225]
	v_add_f32_e32 v232, 1.0, v232
	v_exp_f32_e32 v227, v219
	v_fma_f32 v235, v233, s41, s41
	v_rcp_f32_e32 v232, v232
	v_min_f32_e32 v228, s42, v220
	v_fma_f32 v235, v231, v235, v235
	v_rcp_f32_e32 v235, v235
	v_exp_f32_e32 v229, v221
	v_fma_f32 v231, -v233, v235, v235
	v_fma_f32 v201, v201, v232, v231
	v_exp_f32_e32 v228, v228
	v_min_f32_e32 v231, s42, v201
	v_exp_f32_e32 v231, v231
	v_add_f32_e32 v227, 1.0, v227
	v_add_f32_e32 v232, 1.0, v231
	v_mfma_f32_16x16x32_f16 v[146:149], v[114:117], v[158:161], v[146:149]
	v_fma_f32 v232, v234, v232, v232
	v_fma_f32 v230, v228, s41, s41
	v_rcp_f32_e32 v232, v232
	v_mfma_f32_16x16x32_f16 v[146:149], v[118:121], v[162:165], v[146:149]
	v_fma_mixhi_f16 v246, -v231, v232, v232
	v_rcp_f32_e32 v227, v227
	v_exp_f32_e32 v231, v222
	buffer_load_dwordx4 v[114:117], v189, s[80:83], s46 offen
	buffer_load_dwordx4 v[118:121], v208, s[80:83], s46 offen
	v_exp_f32_e32 v232, v223
	v_fma_f32 v230, v236, v230, v230
	v_min_f32_e32 v233, s42, v224
	s_waitcnt lgkmcnt(0)
	v_mfma_f32_16x16x32_f16 v[210:213], v[70:73], v[150:153], v[98:101]
	v_exp_f32_e32 v234, v225
	v_rcp_f32_e32 v230, v230
	v_exp_f32_e32 v233, v233
	v_mfma_f32_16x16x32_f16 v[214:217], v[74:77], v[150:153], v[102:105]
	v_add_f32_e32 v232, 1.0, v232
	v_fma_f32 v236, -v228, v230, v230
	v_fma_f32 v235, v233, s41, s41
	v_rcp_f32_e32 v232, v232
	v_fma_f32 v198, v198, v227, v236
	v_fma_f32 v235, v231, v235, v235
	v_rcp_f32_e32 v235, v235
	v_min_f32_e32 v236, s42, v198
	v_fma_f32 v231, -v233, v235, v235
	v_fma_f32 v199, v199, v232, v231
	v_exp_f32_e32 v236, v236
	v_min_f32_e32 v231, s42, v199
	v_exp_f32_e32 v231, v231
	v_add_f32_e32 v227, 1.0, v236
	v_add_f32_e32 v232, 1.0, v231
	v_fma_f32 v227, v229, v227, v227
	v_fma_f32 v232, v234, v232, v232
	v_rcp_f32_e32 v227, v227
	v_rcp_f32_e32 v232, v232
	v_fma_mixlo_f16 v247, -v236, v227, v227
	v_fma_mixhi_f16 v247, -v231, v232, v232
	ds_write_b64 v250, v[246:247] offset:8192
	v_mfma_f32_16x16x32_f16 v[210:213], v[66:69], v[154:157], v[210:213]
	v_mfma_f32_16x16x32_f16 v[214:217], v[78:81], v[154:157], v[214:217]
	buffer_load_dwordx2 v[190:191], v209, s[60:63], s45 offen
	s_add_i32 s45, s45, 0x400000
	s_add_i32 s46, s46, 0x10000
	s_waitcnt lgkmcnt(0)
	s_barrier
	ds_read_b128 v[158:161], v248 offset:0
	ds_read_b128 v[162:165], v248 offset:1024
	ds_read_b128 v[166:169], v249 offset:2048
	ds_read_b128 v[170:173], v249 offset:3072
	v_mfma_f32_16x16x32_f16 v[218:221], v[82:85], v[150:153], v[106:109]
	v_mfma_f32_16x16x32_f16 v[222:225], v[90:93], v[150:153], v[110:113]
	v_mfma_f32_16x16x32_f16 v[218:221], v[86:89], v[154:157], v[218:221]
	v_mfma_f32_16x16x32_f16 v[222:225], v[94:97], v[154:157], v[222:225]
	s_waitcnt lgkmcnt(2)
	v_mfma_f32_16x16x32_f16 v[210:213], v[54:57], v[158:161], v[210:213]
	v_mfma_f32_16x16x32_f16 v[210:213], v[58:61], v[162:165], v[210:213]
	s_waitcnt lgkmcnt(0)
	v_mfma_f32_16x16x32_f16 v[210:213], v[62:65], v[166:169], v[210:213]
	v_mfma_f32_16x16x32_f16 v[210:213], v[50:53], v[170:173], v[210:213]
	s_waitcnt vmcnt(9)
	v_cvt_pk_f16_f32 v251, v196, v197
	ds_write_b32 v1, v251 offset:4096
	ds_read_b128 v[150:153], v186 offset:2048
	ds_read_b128 v[154:157], v186 offset:3072
	v_add_u32_e32 v250, 0x1000, v250
	v_add_u32_e32 v248, 0x1000, v248
	v_add_u32_e32 v249, 0x1000, v249
	v_exp_f32_e32 v226, v210
	v_exp_f32_e32 v227, v211
	v_mfma_f32_16x16x32_f16 v[214:217], v[34:37], v[158:161], v[214:217]
	v_min_f32_e32 v228, s42, v212
	v_exp_f32_e32 v229, v213
	v_mfma_f32_16x16x32_f16 v[214:217], v[38:41], v[162:165], v[214:217]
	v_exp_f32_e32 v228, v228
	v_add_f32_e32 v227, 1.0, v227
	v_mfma_f32_16x16x32_f16 v[214:217], v[42:45], v[166:169], v[214:217]
	v_fma_f32 v230, v228, s41, s41
	v_rcp_f32_e32 v227, v227
	v_mfma_f32_16x16x32_f16 v[214:217], v[46:49], v[170:173], v[214:217]
	v_fma_f32 v230, v226, v230, v230
	v_rcp_f32_e32 v230, v230
	v_mfma_f32_16x16x32_f16 v[218:221], v[18:21], v[158:161], v[218:221]
	v_fma_f32 v226, -v228, v230, v230
	v_fma_f32 v200, v200, v227, v226
	v_mfma_f32_16x16x32_f16 v[218:221], v[14:17], v[162:165], v[218:221]
	v_min_f32_e32 v226, s42, v200
	v_exp_f32_e32 v226, v226
	v_mfma_f32_16x16x32_f16 v[218:221], v[10:13], v[166:169], v[218:221]
	v_add_f32_e32 v227, 1.0, v226
	v_fma_f32 v227, v229, v227, v227
	v_mfma_f32_16x16x32_f16 v[218:221], v[26:29], v[170:173], v[218:221]
	v_rcp_f32_e32 v227, v227
	v_exp_f32_e32 v231, v214
	v_mfma_f32_16x16x32_f16 v[222:225], v[2:5], v[158:161], v[222:225]
	v_exp_f32_e32 v232, v215
	v_fma_mixlo_f16 v246, -v226, v227, v227
	v_mfma_f32_16x16x32_f16 v[222:225], v[6:9], v[162:165], v[222:225]
	v_min_f32_e32 v233, s42, v216
	v_exp_f32_e32 v234, v217
	v_mfma_f32_16x16x32_f16 v[222:225], v[22:25], v[166:169], v[222:225]
	v_exp_f32_e32 v236, v218
	v_exp_f32_e32 v233, v233
	v_mfma_f32_16x16x32_f16 v[222:225], v[30:33], v[170:173], v[222:225]
	v_add_f32_e32 v232, 1.0, v232
	v_exp_f32_e32 v227, v219
	v_fma_f32 v235, v233, s41, s41
	v_rcp_f32_e32 v232, v232
	v_min_f32_e32 v228, s42, v220
	v_fma_f32 v235, v231, v235, v235
	v_rcp_f32_e32 v235, v235
	v_exp_f32_e32 v229, v221
	v_fma_f32 v231, -v233, v235, v235
	v_fma_f32 v201, v201, v232, v231
	v_exp_f32_e32 v228, v228
	v_min_f32_e32 v231, s42, v201
	v_exp_f32_e32 v231, v231
	v_add_f32_e32 v227, 1.0, v227
	v_add_f32_e32 v232, 1.0, v231
	v_mfma_f32_16x16x32_f16 v[146:149], v[138:141], v[158:161], v[146:149]
	v_fma_f32 v232, v234, v232, v232
	v_fma_f32 v230, v228, s41, s41
	v_rcp_f32_e32 v232, v232
	v_mfma_f32_16x16x32_f16 v[146:149], v[142:145], v[162:165], v[146:149]
	v_fma_mixhi_f16 v246, -v231, v232, v232
	v_rcp_f32_e32 v227, v227
	v_exp_f32_e32 v231, v222
	buffer_load_dwordx4 v[138:141], v189, s[68:71], s46 offen
	buffer_load_dwordx4 v[142:145], v208, s[68:71], s46 offen
	v_exp_f32_e32 v232, v223
	v_fma_f32 v230, v236, v230, v230
	v_min_f32_e32 v233, s42, v224
	s_waitcnt lgkmcnt(0)
	v_mfma_f32_16x16x32_f16 v[210:213], v[70:73], v[150:153], v[98:101]
	v_exp_f32_e32 v234, v225
	v_rcp_f32_e32 v230, v230
	v_exp_f32_e32 v233, v233
	v_mfma_f32_16x16x32_f16 v[214:217], v[74:77], v[150:153], v[102:105]
	v_add_f32_e32 v232, 1.0, v232
	v_fma_f32 v236, -v228, v230, v230
	v_fma_f32 v235, v233, s41, s41
	v_rcp_f32_e32 v232, v232
	v_fma_f32 v198, v198, v227, v236
	v_fma_f32 v235, v231, v235, v235
	v_rcp_f32_e32 v235, v235
	v_min_f32_e32 v236, s42, v198
	v_fma_f32 v231, -v233, v235, v235
	v_fma_f32 v199, v199, v232, v231
	v_exp_f32_e32 v236, v236
	v_min_f32_e32 v231, s42, v199
	v_exp_f32_e32 v231, v231
	v_add_f32_e32 v227, 1.0, v236
	v_add_f32_e32 v232, 1.0, v231
	v_fma_f32 v227, v229, v227, v227
	v_fma_f32 v232, v234, v232, v232
	v_rcp_f32_e32 v227, v227
	v_rcp_f32_e32 v232, v232
	v_fma_mixlo_f16 v247, -v236, v227, v227
	v_fma_mixhi_f16 v247, -v231, v232, v232
	ds_write_b64 v250, v[246:247] offset:8192
	v_mfma_f32_16x16x32_f16 v[210:213], v[66:69], v[154:157], v[210:213]
	v_mfma_f32_16x16x32_f16 v[214:217], v[78:81], v[154:157], v[214:217]
	buffer_load_dwordx2 v[196:197], v209, s[48:51], s45 offen
	s_waitcnt lgkmcnt(0)
	s_barrier
	ds_read_b128 v[158:161], v248 offset:0
	ds_read_b128 v[162:165], v248 offset:1024
	ds_read_b128 v[166:169], v249 offset:2048
	ds_read_b128 v[170:173], v249 offset:3072
	v_mfma_f32_16x16x32_f16 v[218:221], v[82:85], v[150:153], v[106:109]
	v_mfma_f32_16x16x32_f16 v[222:225], v[90:93], v[150:153], v[110:113]
	v_mfma_f32_16x16x32_f16 v[218:221], v[86:89], v[154:157], v[218:221]
	v_mfma_f32_16x16x32_f16 v[222:225], v[94:97], v[154:157], v[222:225]
	s_waitcnt lgkmcnt(2)
	v_mfma_f32_16x16x32_f16 v[210:213], v[54:57], v[158:161], v[210:213]
	v_mfma_f32_16x16x32_f16 v[210:213], v[58:61], v[162:165], v[210:213]
	s_waitcnt lgkmcnt(0)
	v_mfma_f32_16x16x32_f16 v[210:213], v[62:65], v[166:169], v[210:213]
	v_mfma_f32_16x16x32_f16 v[210:213], v[50:53], v[170:173], v[210:213]
	s_waitcnt vmcnt(9)
	v_cvt_pk_f16_f32 v251, v194, v195
	ds_write_b32 v1, v251 offset:6144
	ds_read_b128 v[150:153], v186 offset:4096
	ds_read_b128 v[154:157], v186 offset:5120
	v_add_u32_e32 v250, 0x1000, v250
	v_add_u32_e32 v248, 0x1000, v248
	v_add_u32_e32 v249, 0x1000, v249
	v_exp_f32_e32 v226, v210
	v_exp_f32_e32 v227, v211
	v_mfma_f32_16x16x32_f16 v[214:217], v[34:37], v[158:161], v[214:217]
	v_min_f32_e32 v228, s42, v212
	v_exp_f32_e32 v229, v213
	v_mfma_f32_16x16x32_f16 v[214:217], v[38:41], v[162:165], v[214:217]
	v_exp_f32_e32 v228, v228
	v_add_f32_e32 v227, 1.0, v227
	v_mfma_f32_16x16x32_f16 v[214:217], v[42:45], v[166:169], v[214:217]
	v_fma_f32 v230, v228, s41, s41
	v_rcp_f32_e32 v227, v227
	v_mfma_f32_16x16x32_f16 v[214:217], v[46:49], v[170:173], v[214:217]
	v_fma_f32 v230, v226, v230, v230
	v_rcp_f32_e32 v230, v230
	v_mfma_f32_16x16x32_f16 v[218:221], v[18:21], v[158:161], v[218:221]
	v_fma_f32 v226, -v228, v230, v230
	v_fma_f32 v200, v200, v227, v226
	v_mfma_f32_16x16x32_f16 v[218:221], v[14:17], v[162:165], v[218:221]
	v_min_f32_e32 v226, s42, v200
	v_exp_f32_e32 v226, v226
	v_mfma_f32_16x16x32_f16 v[218:221], v[10:13], v[166:169], v[218:221]
	v_add_f32_e32 v227, 1.0, v226
	v_fma_f32 v227, v229, v227, v227
	v_mfma_f32_16x16x32_f16 v[218:221], v[26:29], v[170:173], v[218:221]
	v_rcp_f32_e32 v227, v227
	v_exp_f32_e32 v231, v214
	v_mfma_f32_16x16x32_f16 v[222:225], v[2:5], v[158:161], v[222:225]
	v_exp_f32_e32 v232, v215
	v_fma_mixlo_f16 v246, -v226, v227, v227
	v_mfma_f32_16x16x32_f16 v[222:225], v[6:9], v[162:165], v[222:225]
	v_min_f32_e32 v233, s42, v216
	v_exp_f32_e32 v234, v217
	v_mfma_f32_16x16x32_f16 v[222:225], v[22:25], v[166:169], v[222:225]
	v_exp_f32_e32 v236, v218
	v_exp_f32_e32 v233, v233
	v_mfma_f32_16x16x32_f16 v[222:225], v[30:33], v[170:173], v[222:225]
	v_add_f32_e32 v232, 1.0, v232
	v_exp_f32_e32 v227, v219
	v_fma_f32 v235, v233, s41, s41
	v_rcp_f32_e32 v232, v232
	v_min_f32_e32 v228, s42, v220
	v_fma_f32 v235, v231, v235, v235
	v_rcp_f32_e32 v235, v235
	v_exp_f32_e32 v229, v221
	v_fma_f32 v231, -v233, v235, v235
	v_fma_f32 v201, v201, v232, v231
	v_exp_f32_e32 v228, v228
	v_min_f32_e32 v231, s42, v201
	v_exp_f32_e32 v231, v231
	v_add_f32_e32 v227, 1.0, v227
	v_add_f32_e32 v232, 1.0, v231
	v_mfma_f32_16x16x32_f16 v[146:149], v[130:133], v[158:161], v[146:149]
	v_fma_f32 v232, v234, v232, v232
	v_fma_f32 v230, v228, s41, s41
	v_rcp_f32_e32 v232, v232
	v_mfma_f32_16x16x32_f16 v[146:149], v[134:137], v[162:165], v[146:149]
	v_fma_mixhi_f16 v246, -v231, v232, v232
	v_rcp_f32_e32 v227, v227
	v_exp_f32_e32 v231, v222
	buffer_load_dwordx4 v[130:133], v189, s[72:75], s46 offen
	buffer_load_dwordx4 v[134:137], v208, s[72:75], s46 offen
	v_exp_f32_e32 v232, v223
	v_fma_f32 v230, v236, v230, v230
	v_min_f32_e32 v233, s42, v224
	s_waitcnt lgkmcnt(0)
	v_mfma_f32_16x16x32_f16 v[210:213], v[70:73], v[150:153], v[98:101]
	v_exp_f32_e32 v234, v225
	v_rcp_f32_e32 v230, v230
	v_exp_f32_e32 v233, v233
	v_mfma_f32_16x16x32_f16 v[214:217], v[74:77], v[150:153], v[102:105]
	v_add_f32_e32 v232, 1.0, v232
	v_fma_f32 v236, -v228, v230, v230
	v_fma_f32 v235, v233, s41, s41
	v_rcp_f32_e32 v232, v232
	v_fma_f32 v198, v198, v227, v236
	v_fma_f32 v235, v231, v235, v235
	v_rcp_f32_e32 v235, v235
	v_min_f32_e32 v236, s42, v198
	v_fma_f32 v231, -v233, v235, v235
	v_fma_f32 v199, v199, v232, v231
	v_exp_f32_e32 v236, v236
	v_min_f32_e32 v231, s42, v199
	v_exp_f32_e32 v231, v231
	v_add_f32_e32 v227, 1.0, v236
	v_add_f32_e32 v232, 1.0, v231
	v_fma_f32 v227, v229, v227, v227
	v_fma_f32 v232, v234, v232, v232
	v_rcp_f32_e32 v227, v227
	v_rcp_f32_e32 v232, v232
	v_fma_mixlo_f16 v247, -v236, v227, v227
	v_fma_mixhi_f16 v247, -v231, v232, v232
	ds_write_b64 v250, v[246:247] offset:8192
	v_mfma_f32_16x16x32_f16 v[210:213], v[66:69], v[154:157], v[210:213]
	v_mfma_f32_16x16x32_f16 v[214:217], v[78:81], v[154:157], v[214:217]
	buffer_load_dwordx2 v[194:195], v209, s[52:55], s45 offen
	s_waitcnt lgkmcnt(0)
	s_barrier
	s_cmp_lt_u32 s46, 0xc0000
	s_cbranch_scc1 .Lmy_loopb
	s_nop 7
	ds_read_b128 v[158:161], v248 offset:0
	ds_read_b128 v[162:165], v248 offset:1024
	s_lshr_b32 s48, s35, 5
	v_and_b32_e32 v211, 15, v0
	v_bfe_u32 v212, v0, 4, 2
	v_and_b32_e32 v213, 31, v0
	v_bfe_u32 v214, v0, 5, 1
	v_add_u32_e32 v214, s48, v214
	s_lshl_b32 s49, s35, 4
	s_addk_i32 s49, 0x2000
	v_lshl_add_u32 v215, v212, 8, s49
	v_lshl_add_u32 v215, v211, 2, v215
	v_lshlrev_b32_e32 v216, 6, v213
	v_lshl_add_u32 v216, v214, 2, v216
	v_mul_u32_u24_e32 v217, 0x110, v214
	v_lshl_add_u32 v217, v213, 2, v217
	v_mul_u32_u24_e32 v218, 0x110, v211
	v_add_u32_e32 v219, 0x4000, v206
	v_add_u32_e32 v220, 0x14000, v206
	v_add_u32_e32 v221, 0x24000, v206
	v_add_u32_e32 v222, s34, v211
	v_lshlrev_b32_e32 v222, 9, v222
	v_add_u32_e32 v222, s35, v222
	v_lshl_add_u32 v222, v212, 4, v222
	s_waitcnt vmcnt(10) lgkmcnt(0)
	v_mfma_f32_16x16x32_f16 v[146:149], v[122:125], v[158:161], v[146:149]
	v_mfma_f32_16x16x32_f16 v[146:149], v[126:129], v[162:165], v[146:149]
	ds_read_b64 v[30:31], v219 offset:0
	ds_read_b64 v[32:33], v219 offset:4096
	ds_read_b64 v[34:35], v219 offset:8192
	ds_read_b64 v[36:37], v219 offset:12288
	ds_read_b64 v[38:39], v219 offset:16384
	ds_read_b64 v[40:41], v219 offset:20480
	ds_read_b64 v[42:43], v219 offset:24576
	ds_read_b64 v[44:45], v219 offset:28672
	s_waitcnt lgkmcnt(4)
	ds_read_b64 v[46:47], v219 offset:32768
	ds_read_b64 v[48:49], v219 offset:36864
	ds_read_b64 v[50:51], v219 offset:40960
	ds_read_b64 v[52:53], v219 offset:45056
	ds_read_b64 v[54:55], v219 offset:49152
	ds_read_b64 v[56:57], v219 offset:53248
	ds_read_b64 v[58:59], v219 offset:57344
	ds_read_b64 v[60:61], v219 offset:61440
	s_waitcnt lgkmcnt(4)
	ds_read_b64 v[62:63], v220 offset:0
	ds_read_b64 v[64:65], v220 offset:4096
	ds_read_b64 v[66:67], v220 offset:8192
	ds_read_b64 v[68:69], v220 offset:12288
	ds_read_b64 v[70:71], v220 offset:16384
	ds_read_b64 v[72:73], v220 offset:20480
	ds_read_b64 v[74:75], v220 offset:24576
	ds_read_b64 v[76:77], v220 offset:28672
	s_waitcnt lgkmcnt(4)
	ds_read_b64 v[78:79], v220 offset:32768
	ds_read_b64 v[80:81], v220 offset:36864
	ds_read_b64 v[82:83], v220 offset:40960
	ds_read_b64 v[84:85], v220 offset:45056
	ds_read_b64 v[86:87], v220 offset:49152
	ds_read_b64 v[88:89], v220 offset:53248
	ds_read_b64 v[90:91], v220 offset:57344
	ds_read_b64 v[92:93], v220 offset:61440
	s_waitcnt lgkmcnt(4)
	ds_read_b64 v[94:95], v221 offset:0
	ds_read_b64 v[96:97], v221 offset:4096
	ds_read_b64 v[98:99], v221 offset:8192
	ds_read_b64 v[100:101], v221 offset:12288
	ds_write2_b32 v215, v146, v147 offset1:16
	ds_write2_b32 v215, v148, v149 offset0:32 offset1:48
	s_waitcnt lgkmcnt(0)
	s_barrier
	ds_read2st64_b32 v[230:231], v216 offset0:32 offset1:48
	ds_read2st64_b32 v[232:233], v216 offset0:40 offset1:56
	v_cmp_gt_u32_e32 vcc, 18, v213
	s_waitcnt vmcnt(0) lgkmcnt(0)
	v_add_f32_e32 v223, v230, v231
	v_add_f32_e32 v224, v232, v233
	v_add_f32_e32 v223, v223, v254
	v_add_f32_e32 v224, v224, v255
	v_max_f32_e32 v223, 0, v223
	v_max_f32_e32 v224, 0, v224
	v_mov_b32_e32 v226, 0xf149f2ca
	v_cndmask_b32_e32 v224, v226, v224, vcc
	v_max_f32_e32 v225, v223, v224
	s_nop 1
	v_max_f32_dpp v226, v225, v225 quad_perm:[1,0,3,2] row_mask:0xf bank_mask:0xf
	s_nop 1
	v_max_f32_dpp v225, v226, v226 quad_perm:[2,3,0,1] row_mask:0xf bank_mask:0xf
	s_nop 1
	v_max_f32_dpp v226, v225, v225 row_half_mirror row_mask:0xf bank_mask:0xf
	s_nop 1
	v_max_f32_dpp v225, v226, v226 row_mirror row_mask:0xf bank_mask:0xf
	ds_swizzle_b32 v226, v225 offset:swizzle(SWAP,16)
	s_waitcnt lgkmcnt(0)
	v_max_f32_e32 v225, v225, v226
	v_sub_f32_e32 v223, v223, v225
	v_sub_f32_e32 v224, v224, v225
	v_mul_f32_e32 v223, 0x3fb8aa3b, v223
	v_mul_f32_e32 v224, 0x3fb8aa3b, v224
	v_exp_f32_e32 v227, v223
	v_exp_f32_e32 v228, v224
	s_nop 0
	v_add_f32_e32 v229, v227, v228
	s_nop 1
	v_add_f32_dpp v226, v229, v229 quad_perm:[1,0,3,2] row_mask:0xf bank_mask:0xf
	s_nop 1
	v_add_f32_dpp v229, v226, v226 quad_perm:[2,3,0,1] row_mask:0xf bank_mask:0xf
	s_nop 1
	v_add_f32_dpp v226, v229, v229 row_half_mirror row_mask:0xf bank_mask:0xf
	s_nop 1
	v_add_f32_dpp v229, v226, v226 row_mirror row_mask:0xf bank_mask:0xf
	ds_swizzle_b32 v226, v229 offset:swizzle(SWAP,16)
	s_waitcnt lgkmcnt(0)
	v_add_f32_e32 v229, v229, v226
	v_rcp_f32_e32 v234, v229
	s_nop 0
	v_mul_f32_e32 v227, v227, v234
	v_mul_f32_e32 v228, v228, v234
	ds_write_b32 v217, v227
	ds_write_b32 v217, v228 offset:128
	s_waitcnt lgkmcnt(0)
	s_barrier
	ds_read_b128 v[102:105], v218 offset:0
	ds_read_b128 v[106:109], v218 offset:16
	ds_read_b128 v[110:113], v218 offset:32
	ds_read_b128 v[114:117], v218 offset:48
	ds_read_b128 v[118:121], v218 offset:64
	ds_read_b128 v[122:125], v218 offset:80
	ds_read_b128 v[126:129], v218 offset:96
	ds_read_b128 v[130:133], v218 offset:112
	ds_read_b128 v[134:137], v218 offset:128
	ds_read_b128 v[138:141], v218 offset:144
	ds_read_b128 v[142:145], v218 offset:160
	ds_read_b128 v[146:149], v218 offset:176
	ds_read_b128 v[150:153], v218 offset:192
	v_mov_b32_e32 v154, 0
	v_mov_b32_e32 v155, 0
	v_mov_b32_e32 v156, 0
	v_mov_b32_e32 v157, 0
	s_waitcnt vmcnt(0) lgkmcnt(0)
	v_fma_mix_f32 v154, v174, v102, v154 op_sel_hi:[1,0,0]
	v_fma_mix_f32 v155, v174, v102, v155 op_sel:[1,0,0] op_sel_hi:[1,0,0]
	v_fma_mix_f32 v156, v175, v102, v156 op_sel_hi:[1,0,0]
	v_fma_mix_f32 v157, v175, v102, v157 op_sel:[1,0,0] op_sel_hi:[1,0,0]
	v_fma_mix_f32 v154, v176, v103, v154 op_sel_hi:[1,0,0]
	v_fma_mix_f32 v155, v176, v103, v155 op_sel:[1,0,0] op_sel_hi:[1,0,0]
	v_fma_mix_f32 v156, v177, v103, v156 op_sel_hi:[1,0,0]
	v_fma_mix_f32 v157, v177, v103, v157 op_sel:[1,0,0] op_sel_hi:[1,0,0]
	v_fma_mix_f32 v154, v178, v104, v154 op_sel_hi:[1,0,0]
	v_fma_mix_f32 v155, v178, v104, v155 op_sel:[1,0,0] op_sel_hi:[1,0,0]
	v_fma_mix_f32 v156, v179, v104, v156 op_sel_hi:[1,0,0]
	v_fma_mix_f32 v157, v179, v104, v157 op_sel:[1,0,0] op_sel_hi:[1,0,0]
	v_fma_mix_f32 v154, v180, v105, v154 op_sel_hi:[1,0,0]
	v_fma_mix_f32 v155, v180, v105, v155 op_sel:[1,0,0] op_sel_hi:[1,0,0]
	v_fma_mix_f32 v156, v181, v105, v156 op_sel_hi:[1,0,0]
	v_fma_mix_f32 v157, v181, v105, v157 op_sel:[1,0,0] op_sel_hi:[1,0,0]
	v_fma_mix_f32 v154, v182, v106, v154 op_sel_hi:[1,0,0]
	v_fma_mix_f32 v155, v182, v106, v155 op_sel:[1,0,0] op_sel_hi:[1,0,0]
	v_fma_mix_f32 v156, v183, v106, v156 op_sel_hi:[1,0,0]
	v_fma_mix_f32 v157, v183, v106, v157 op_sel:[1,0,0] op_sel_hi:[1,0,0]
	v_fma_mix_f32 v154, v184, v107, v154 op_sel_hi:[1,0,0]
	v_fma_mix_f32 v155, v184, v107, v155 op_sel:[1,0,0] op_sel_hi:[1,0,0]
	v_fma_mix_f32 v156, v185, v107, v156 op_sel_hi:[1,0,0]
	v_fma_mix_f32 v157, v185, v107, v157 op_sel:[1,0,0] op_sel_hi:[1,0,0]
	v_fma_mix_f32 v154, v237, v108, v154 op_sel_hi:[1,0,0]
	v_fma_mix_f32 v155, v237, v108, v155 op_sel:[1,0,0] op_sel_hi:[1,0,0]
	v_fma_mix_f32 v156, v238, v108, v156 op_sel_hi:[1,0,0]
	v_fma_mix_f32 v157, v238, v108, v157 op_sel:[1,0,0] op_sel_hi:[1,0,0]
	v_fma_mix_f32 v154, v239, v109, v154 op_sel_hi:[1,0,0]
	v_fma_mix_f32 v155, v239, v109, v155 op_sel:[1,0,0] op_sel_hi:[1,0,0]
	v_fma_mix_f32 v156, v240, v109, v156 op_sel_hi:[1,0,0]
	v_fma_mix_f32 v157, v240, v109, v157 op_sel:[1,0,0] op_sel_hi:[1,0,0]
	v_fma_mix_f32 v154, v241, v110, v154 op_sel_hi:[1,0,0]
	v_fma_mix_f32 v155, v241, v110, v155 op_sel:[1,0,0] op_sel_hi:[1,0,0]
	v_fma_mix_f32 v156, v242, v110, v156 op_sel_hi:[1,0,0]
	v_fma_mix_f32 v157, v242, v110, v157 op_sel:[1,0,0] op_sel_hi:[1,0,0]
	v_fma_mix_f32 v154, v243, v111, v154 op_sel_hi:[1,0,0]
	v_fma_mix_f32 v155, v243, v111, v155 op_sel:[1,0,0] op_sel_hi:[1,0,0]
	v_fma_mix_f32 v156, v244, v111, v156 op_sel_hi:[1,0,0]
	v_fma_mix_f32 v157, v244, v111, v157 op_sel:[1,0,0] op_sel_hi:[1,0,0]
	v_fma_mix_f32 v154, v245, v112, v154 op_sel_hi:[1,0,0]
	v_fma_mix_f32 v155, v245, v112, v155 op_sel:[1,0,0] op_sel_hi:[1,0,0]
	v_fma_mix_f32 v156, v187, v112, v156 op_sel_hi:[1,0,0]
	v_fma_mix_f32 v157, v187, v112, v157 op_sel:[1,0,0] op_sel_hi:[1,0,0]
	v_fma_mix_f32 v154, v188, v113, v154 op_sel_hi:[1,0,0]
	v_fma_mix_f32 v155, v188, v113, v155 op_sel:[1,0,0] op_sel_hi:[1,0,0]
	v_fma_mix_f32 v156, v202, v113, v156 op_sel_hi:[1,0,0]
	v_fma_mix_f32 v157, v202, v113, v157 op_sel:[1,0,0] op_sel_hi:[1,0,0]
	v_fma_mix_f32 v154, v203, v114, v154 op_sel_hi:[1,0,0]
	v_fma_mix_f32 v155, v203, v114, v155 op_sel:[1,0,0] op_sel_hi:[1,0,0]
	v_fma_mix_f32 v156, v204, v114, v156 op_sel_hi:[1,0,0]
	v_fma_mix_f32 v157, v204, v114, v157 op_sel:[1,0,0] op_sel_hi:[1,0,0]
	v_fma_mix_f32 v154, v205, v115, v154 op_sel_hi:[1,0,0]
	v_fma_mix_f32 v155, v205, v115, v155 op_sel:[1,0,0] op_sel_hi:[1,0,0]
	v_fma_mix_f32 v156, v207, v115, v156 op_sel_hi:[1,0,0]
	v_fma_mix_f32 v157, v207, v115, v157 op_sel:[1,0,0] op_sel_hi:[1,0,0]
	v_fma_mix_f32 v154, v30, v116, v154 op_sel_hi:[1,0,0]
	v_fma_mix_f32 v155, v30, v116, v155 op_sel:[1,0,0] op_sel_hi:[1,0,0]
	v_fma_mix_f32 v156, v31, v116, v156 op_sel_hi:[1,0,0]
	v_fma_mix_f32 v157, v31, v116, v157 op_sel:[1,0,0] op_sel_hi:[1,0,0]
	v_fma_mix_f32 v154, v32, v117, v154 op_sel_hi:[1,0,0]
	v_fma_mix_f32 v155, v32, v117, v155 op_sel:[1,0,0] op_sel_hi:[1,0,0]
	v_fma_mix_f32 v156, v33, v117, v156 op_sel_hi:[1,0,0]
	v_fma_mix_f32 v157, v33, v117, v157 op_sel:[1,0,0] op_sel_hi:[1,0,0]
	v_fma_mix_f32 v154, v34, v118, v154 op_sel_hi:[1,0,0]
	v_fma_mix_f32 v155, v34, v118, v155 op_sel:[1,0,0] op_sel_hi:[1,0,0]
	v_fma_mix_f32 v156, v35, v118, v156 op_sel_hi:[1,0,0]
	v_fma_mix_f32 v157, v35, v118, v157 op_sel:[1,0,0] op_sel_hi:[1,0,0]
	v_fma_mix_f32 v154, v36, v119, v154 op_sel_hi:[1,0,0]
	v_fma_mix_f32 v155, v36, v119, v155 op_sel:[1,0,0] op_sel_hi:[1,0,0]
	v_fma_mix_f32 v156, v37, v119, v156 op_sel_hi:[1,0,0]
	v_fma_mix_f32 v157, v37, v119, v157 op_sel:[1,0,0] op_sel_hi:[1,0,0]
	v_fma_mix_f32 v154, v38, v120, v154 op_sel_hi:[1,0,0]
	v_fma_mix_f32 v155, v38, v120, v155 op_sel:[1,0,0] op_sel_hi:[1,0,0]
	v_fma_mix_f32 v156, v39, v120, v156 op_sel_hi:[1,0,0]
	v_fma_mix_f32 v157, v39, v120, v157 op_sel:[1,0,0] op_sel_hi:[1,0,0]
	v_fma_mix_f32 v154, v40, v121, v154 op_sel_hi:[1,0,0]
	v_fma_mix_f32 v155, v40, v121, v155 op_sel:[1,0,0] op_sel_hi:[1,0,0]
	v_fma_mix_f32 v156, v41, v121, v156 op_sel_hi:[1,0,0]
	v_fma_mix_f32 v157, v41, v121, v157 op_sel:[1,0,0] op_sel_hi:[1,0,0]
	v_fma_mix_f32 v154, v42, v122, v154 op_sel_hi:[1,0,0]
	v_fma_mix_f32 v155, v42, v122, v155 op_sel:[1,0,0] op_sel_hi:[1,0,0]
	v_fma_mix_f32 v156, v43, v122, v156 op_sel_hi:[1,0,0]
	v_fma_mix_f32 v157, v43, v122, v157 op_sel:[1,0,0] op_sel_hi:[1,0,0]
	v_fma_mix_f32 v154, v44, v123, v154 op_sel_hi:[1,0,0]
	v_fma_mix_f32 v155, v44, v123, v155 op_sel:[1,0,0] op_sel_hi:[1,0,0]
	v_fma_mix_f32 v156, v45, v123, v156 op_sel_hi:[1,0,0]
	v_fma_mix_f32 v157, v45, v123, v157 op_sel:[1,0,0] op_sel_hi:[1,0,0]
	v_fma_mix_f32 v154, v46, v124, v154 op_sel_hi:[1,0,0]
	v_fma_mix_f32 v155, v46, v124, v155 op_sel:[1,0,0] op_sel_hi:[1,0,0]
	v_fma_mix_f32 v156, v47, v124, v156 op_sel_hi:[1,0,0]
	v_fma_mix_f32 v157, v47, v124, v157 op_sel:[1,0,0] op_sel_hi:[1,0,0]
	v_fma_mix_f32 v154, v48, v125, v154 op_sel_hi:[1,0,0]
	v_fma_mix_f32 v155, v48, v125, v155 op_sel:[1,0,0] op_sel_hi:[1,0,0]
	v_fma_mix_f32 v156, v49, v125, v156 op_sel_hi:[1,0,0]
	v_fma_mix_f32 v157, v49, v125, v157 op_sel:[1,0,0] op_sel_hi:[1,0,0]
	v_fma_mix_f32 v154, v50, v126, v154 op_sel_hi:[1,0,0]
	v_fma_mix_f32 v155, v50, v126, v155 op_sel:[1,0,0] op_sel_hi:[1,0,0]
	v_fma_mix_f32 v156, v51, v126, v156 op_sel_hi:[1,0,0]
	v_fma_mix_f32 v157, v51, v126, v157 op_sel:[1,0,0] op_sel_hi:[1,0,0]
	v_fma_mix_f32 v154, v52, v127, v154 op_sel_hi:[1,0,0]
	v_fma_mix_f32 v155, v52, v127, v155 op_sel:[1,0,0] op_sel_hi:[1,0,0]
	v_fma_mix_f32 v156, v53, v127, v156 op_sel_hi:[1,0,0]
	v_fma_mix_f32 v157, v53, v127, v157 op_sel:[1,0,0] op_sel_hi:[1,0,0]
	v_fma_mix_f32 v154, v54, v128, v154 op_sel_hi:[1,0,0]
	v_fma_mix_f32 v155, v54, v128, v155 op_sel:[1,0,0] op_sel_hi:[1,0,0]
	v_fma_mix_f32 v156, v55, v128, v156 op_sel_hi:[1,0,0]
	v_fma_mix_f32 v157, v55, v128, v157 op_sel:[1,0,0] op_sel_hi:[1,0,0]
	v_fma_mix_f32 v154, v56, v129, v154 op_sel_hi:[1,0,0]
	v_fma_mix_f32 v155, v56, v129, v155 op_sel:[1,0,0] op_sel_hi:[1,0,0]
	v_fma_mix_f32 v156, v57, v129, v156 op_sel_hi:[1,0,0]
	v_fma_mix_f32 v157, v57, v129, v157 op_sel:[1,0,0] op_sel_hi:[1,0,0]
	v_fma_mix_f32 v154, v58, v130, v154 op_sel_hi:[1,0,0]
	v_fma_mix_f32 v155, v58, v130, v155 op_sel:[1,0,0] op_sel_hi:[1,0,0]
	v_fma_mix_f32 v156, v59, v130, v156 op_sel_hi:[1,0,0]
	v_fma_mix_f32 v157, v59, v130, v157 op_sel:[1,0,0] op_sel_hi:[1,0,0]
	v_fma_mix_f32 v154, v60, v131, v154 op_sel_hi:[1,0,0]
	v_fma_mix_f32 v155, v60, v131, v155 op_sel:[1,0,0] op_sel_hi:[1,0,0]
	v_fma_mix_f32 v156, v61, v131, v156 op_sel_hi:[1,0,0]
	v_fma_mix_f32 v157, v61, v131, v157 op_sel:[1,0,0] op_sel_hi:[1,0,0]
	v_fma_mix_f32 v154, v62, v132, v154 op_sel_hi:[1,0,0]
	v_fma_mix_f32 v155, v62, v132, v155 op_sel:[1,0,0] op_sel_hi:[1,0,0]
	v_fma_mix_f32 v156, v63, v132, v156 op_sel_hi:[1,0,0]
	v_fma_mix_f32 v157, v63, v132, v157 op_sel:[1,0,0] op_sel_hi:[1,0,0]
	v_fma_mix_f32 v154, v64, v133, v154 op_sel_hi:[1,0,0]
	v_fma_mix_f32 v155, v64, v133, v155 op_sel:[1,0,0] op_sel_hi:[1,0,0]
	v_fma_mix_f32 v156, v65, v133, v156 op_sel_hi:[1,0,0]
	v_fma_mix_f32 v157, v65, v133, v157 op_sel:[1,0,0] op_sel_hi:[1,0,0]
	v_fma_mix_f32 v154, v66, v134, v154 op_sel_hi:[1,0,0]
	v_fma_mix_f32 v155, v66, v134, v155 op_sel:[1,0,0] op_sel_hi:[1,0,0]
	v_fma_mix_f32 v156, v67, v134, v156 op_sel_hi:[1,0,0]
	v_fma_mix_f32 v157, v67, v134, v157 op_sel:[1,0,0] op_sel_hi:[1,0,0]
	v_fma_mix_f32 v154, v68, v135, v154 op_sel_hi:[1,0,0]
	v_fma_mix_f32 v155, v68, v135, v155 op_sel:[1,0,0] op_sel_hi:[1,0,0]
	v_fma_mix_f32 v156, v69, v135, v156 op_sel_hi:[1,0,0]
	v_fma_mix_f32 v157, v69, v135, v157 op_sel:[1,0,0] op_sel_hi:[1,0,0]
	v_fma_mix_f32 v154, v70, v136, v154 op_sel_hi:[1,0,0]
	v_fma_mix_f32 v155, v70, v136, v155 op_sel:[1,0,0] op_sel_hi:[1,0,0]
	v_fma_mix_f32 v156, v71, v136, v156 op_sel_hi:[1,0,0]
	v_fma_mix_f32 v157, v71, v136, v157 op_sel:[1,0,0] op_sel_hi:[1,0,0]
	v_fma_mix_f32 v154, v72, v137, v154 op_sel_hi:[1,0,0]
	v_fma_mix_f32 v155, v72, v137, v155 op_sel:[1,0,0] op_sel_hi:[1,0,0]
	v_fma_mix_f32 v156, v73, v137, v156 op_sel_hi:[1,0,0]
	v_fma_mix_f32 v157, v73, v137, v157 op_sel:[1,0,0] op_sel_hi:[1,0,0]
	v_fma_mix_f32 v154, v74, v138, v154 op_sel_hi:[1,0,0]
	v_fma_mix_f32 v155, v74, v138, v155 op_sel:[1,0,0] op_sel_hi:[1,0,0]
	v_fma_mix_f32 v156, v75, v138, v156 op_sel_hi:[1,0,0]
	v_fma_mix_f32 v157, v75, v138, v157 op_sel:[1,0,0] op_sel_hi:[1,0,0]
	v_fma_mix_f32 v154, v76, v139, v154 op_sel_hi:[1,0,0]
	v_fma_mix_f32 v155, v76, v139, v155 op_sel:[1,0,0] op_sel_hi:[1,0,0]
	v_fma_mix_f32 v156, v77, v139, v156 op_sel_hi:[1,0,0]
	v_fma_mix_f32 v157, v77, v139, v157 op_sel:[1,0,0] op_sel_hi:[1,0,0]
	v_fma_mix_f32 v154, v78, v140, v154 op_sel_hi:[1,0,0]
	v_fma_mix_f32 v155, v78, v140, v155 op_sel:[1,0,0] op_sel_hi:[1,0,0]
	v_fma_mix_f32 v156, v79, v140, v156 op_sel_hi:[1,0,0]
	v_fma_mix_f32 v157, v79, v140, v157 op_sel:[1,0,0] op_sel_hi:[1,0,0]
	v_fma_mix_f32 v154, v80, v141, v154 op_sel_hi:[1,0,0]
	v_fma_mix_f32 v155, v80, v141, v155 op_sel:[1,0,0] op_sel_hi:[1,0,0]
	v_fma_mix_f32 v156, v81, v141, v156 op_sel_hi:[1,0,0]
	v_fma_mix_f32 v157, v81, v141, v157 op_sel:[1,0,0] op_sel_hi:[1,0,0]
	v_fma_mix_f32 v154, v82, v142, v154 op_sel_hi:[1,0,0]
	v_fma_mix_f32 v155, v82, v142, v155 op_sel:[1,0,0] op_sel_hi:[1,0,0]
	v_fma_mix_f32 v156, v83, v142, v156 op_sel_hi:[1,0,0]
	v_fma_mix_f32 v157, v83, v142, v157 op_sel:[1,0,0] op_sel_hi:[1,0,0]
	v_fma_mix_f32 v154, v84, v143, v154 op_sel_hi:[1,0,0]
	v_fma_mix_f32 v155, v84, v143, v155 op_sel:[1,0,0] op_sel_hi:[1,0,0]
	v_fma_mix_f32 v156, v85, v143, v156 op_sel_hi:[1,0,0]
	v_fma_mix_f32 v157, v85, v143, v157 op_sel:[1,0,0] op_sel_hi:[1,0,0]
	v_fma_mix_f32 v154, v86, v144, v154 op_sel_hi:[1,0,0]
	v_fma_mix_f32 v155, v86, v144, v155 op_sel:[1,0,0] op_sel_hi:[1,0,0]
	v_fma_mix_f32 v156, v87, v144, v156 op_sel_hi:[1,0,0]
	v_fma_mix_f32 v157, v87, v144, v157 op_sel:[1,0,0] op_sel_hi:[1,0,0]
	v_fma_mix_f32 v154, v88, v145, v154 op_sel_hi:[1,0,0]
	v_fma_mix_f32 v155, v88, v145, v155 op_sel:[1,0,0] op_sel_hi:[1,0,0]
	v_fma_mix_f32 v156, v89, v145, v156 op_sel_hi:[1,0,0]
	v_fma_mix_f32 v157, v89, v145, v157 op_sel:[1,0,0] op_sel_hi:[1,0,0]
	v_fma_mix_f32 v154, v90, v146, v154 op_sel_hi:[1,0,0]
	v_fma_mix_f32 v155, v90, v146, v155 op_sel:[1,0,0] op_sel_hi:[1,0,0]
	v_fma_mix_f32 v156, v91, v146, v156 op_sel_hi:[1,0,0]
	v_fma_mix_f32 v157, v91, v146, v157 op_sel:[1,0,0] op_sel_hi:[1,0,0]
	v_fma_mix_f32 v154, v92, v147, v154 op_sel_hi:[1,0,0]
	v_fma_mix_f32 v155, v92, v147, v155 op_sel:[1,0,0] op_sel_hi:[1,0,0]
	v_fma_mix_f32 v156, v93, v147, v156 op_sel_hi:[1,0,0]
	v_fma_mix_f32 v157, v93, v147, v157 op_sel:[1,0,0] op_sel_hi:[1,0,0]
	v_fma_mix_f32 v154, v94, v148, v154 op_sel_hi:[1,0,0]
	v_fma_mix_f32 v155, v94, v148, v155 op_sel:[1,0,0] op_sel_hi:[1,0,0]
	v_fma_mix_f32 v156, v95, v148, v156 op_sel_hi:[1,0,0]
	v_fma_mix_f32 v157, v95, v148, v157 op_sel:[1,0,0] op_sel_hi:[1,0,0]
	v_fma_mix_f32 v154, v96, v149, v154 op_sel_hi:[1,0,0]
	v_fma_mix_f32 v155, v96, v149, v155 op_sel:[1,0,0] op_sel_hi:[1,0,0]
	v_fma_mix_f32 v156, v97, v149, v156 op_sel_hi:[1,0,0]
	v_fma_mix_f32 v157, v97, v149, v157 op_sel:[1,0,0] op_sel_hi:[1,0,0]
	v_fma_mix_f32 v154, v98, v150, v154 op_sel_hi:[1,0,0]
	v_fma_mix_f32 v155, v98, v150, v155 op_sel:[1,0,0] op_sel_hi:[1,0,0]
	v_fma_mix_f32 v156, v99, v150, v156 op_sel_hi:[1,0,0]
	v_fma_mix_f32 v157, v99, v150, v157 op_sel:[1,0,0] op_sel_hi:[1,0,0]
	v_fma_mix_f32 v154, v100, v151, v154 op_sel_hi:[1,0,0]
	v_fma_mix_f32 v155, v100, v151, v155 op_sel:[1,0,0] op_sel_hi:[1,0,0]
	v_fma_mix_f32 v156, v101, v151, v156 op_sel_hi:[1,0,0]
	v_fma_mix_f32 v157, v101, v151, v157 op_sel:[1,0,0] op_sel_hi:[1,0,0]
	global_store_dwordx4 v222, v[154:157], s[8:9]
	s_endpgm
